# GEMM phases: branch around the redundant accumulator copy block before each unit K-loop (17 phases)
# speedup vs baseline: 1.0039x; 1.0020x over previous
;     __device__ __forceinline__ void operator()(const f32x4 (&acc)[2][2][4][2], const Unit& u, int wr, int wc, int fr, int fq) const {
;     ...
;         for (int n = 0; n < 2; ++n) { cg[n] = IN8 ? *(const f32x4*)(cstep + u.pn * BM + wc * 32 + 8 * fq + 4 * n) : (f32x4){1.f, 1.f, 1.f, 1.f}; cu[n] = IN8 ? *(const f32x4*)(cstep + u.pn * BM + HALF + wc * 32 + 8 * fq + 4 * n) : (f32x4){1.f, 1.f, 1.f, 1.f}; }
;     ...
; #pragma unroll
;         for (int a = 0; a < 2; ++a)
; #pragma unroll
;             for (int b = 0; b < 2; ++b)
; #pragma unroll
;                 for (int m = 0; m < 4; ++m)
; #pragma unroll
;                     for (int n = 0; n < 2; ++n) acc[a][b][m][n] = (f32x4){0.f, 0.f, 0.f, 0.f};
.LBB0_225:
	s_ashr_i32 s17, s16, 31
	s_lshl_b64 s[18:19], s[16:17], 19
	s_add_u32 s18, s37, s18
	s_addc_u32 s19, s38, s19
	s_ashr_i32 s15, s14, 31
	s_lshl_b64 s[20:21], s[14:15], 19
	s_add_u32 s20, s39, s20
	v_mov_b32_e32 v129, 0
	s_addc_u32 s21, s40, s21
	s_andn2_b64 vcc, exec, s[10:11]
	s_cbranch_vccz .Lzs_1
	v_mov_b32_e32 v128, v129
	v_mov_b32_e32 v127, v129
	v_mov_b32_e32 v126, v129
	v_mov_b32_e32 v121, v129
	v_mov_b32_e32 v120, v129
	v_mov_b32_e32 v119, v129
	v_mov_b32_e32 v118, v129
	v_mov_b32_e32 v113, v129
	v_mov_b32_e32 v112, v129
	v_mov_b32_e32 v111, v129
	v_mov_b32_e32 v110, v129
	v_mov_b32_e32 v105, v129
	v_mov_b32_e32 v104, v129
	v_mov_b32_e32 v103, v129
	v_mov_b32_e32 v102, v129
	v_mov_b32_e32 v97, v129
	v_mov_b32_e32 v96, v129
	v_mov_b32_e32 v95, v129
	v_mov_b32_e32 v94, v129
	v_mov_b32_e32 v89, v129
	v_mov_b32_e32 v88, v129
	v_mov_b32_e32 v87, v129
	v_mov_b32_e32 v86, v129
	v_mov_b32_e32 v81, v129
	v_mov_b32_e32 v80, v129
	v_mov_b32_e32 v79, v129
	v_mov_b32_e32 v78, v129
	v_mov_b32_e32 v73, v129
	v_mov_b32_e32 v72, v129
	v_mov_b32_e32 v71, v129
	v_mov_b32_e32 v70, v129
	v_mov_b32_e32 v125, v129
	v_mov_b32_e32 v124, v129
	v_mov_b32_e32 v123, v129
	v_mov_b32_e32 v122, v129
	v_mov_b32_e32 v117, v129
	v_mov_b32_e32 v116, v129
	v_mov_b32_e32 v115, v129
	v_mov_b32_e32 v114, v129
	v_mov_b32_e32 v109, v129
	v_mov_b32_e32 v108, v129
	v_mov_b32_e32 v107, v129
	v_mov_b32_e32 v106, v129
	v_mov_b32_e32 v101, v129
	v_mov_b32_e32 v100, v129
	v_mov_b32_e32 v99, v129
	v_mov_b32_e32 v98, v129
	v_mov_b32_e32 v93, v129
	v_mov_b32_e32 v92, v129
	v_mov_b32_e32 v91, v129
	v_mov_b32_e32 v90, v129
	v_mov_b32_e32 v85, v129
	v_mov_b32_e32 v84, v129
	v_mov_b32_e32 v83, v129
	v_mov_b32_e32 v82, v129
	v_mov_b32_e32 v77, v129
	v_mov_b32_e32 v76, v129
	v_mov_b32_e32 v75, v129
	v_mov_b32_e32 v74, v129
	v_mov_b32_e32 v69, v129
	v_mov_b32_e32 v68, v129
	v_mov_b32_e32 v67, v129
	v_mov_b32_e32 v66, v129
	v_mov_b32_e32 v65, v129
	v_mov_b32_e32 v64, v129
	v_mov_b32_e32 v63, v129
	v_mov_b32_e32 v62, v129
	v_mov_b32_e32 v57, v129
	v_mov_b32_e32 v56, v129
	v_mov_b32_e32 v55, v129
	v_mov_b32_e32 v54, v129
	v_mov_b32_e32 v49, v129
	v_mov_b32_e32 v48, v129
	v_mov_b32_e32 v47, v129
	v_mov_b32_e32 v46, v129
	v_mov_b32_e32 v41, v129
	v_mov_b32_e32 v40, v129
	v_mov_b32_e32 v39, v129
	v_mov_b32_e32 v38, v129
	v_mov_b32_e32 v33, v129
	v_mov_b32_e32 v32, v129
	v_mov_b32_e32 v31, v129
	v_mov_b32_e32 v30, v129
	v_mov_b32_e32 v25, v129
	v_mov_b32_e32 v24, v129
	v_mov_b32_e32 v23, v129
	v_mov_b32_e32 v22, v129
	v_mov_b32_e32 v17, v129
	v_mov_b32_e32 v16, v129
	v_mov_b32_e32 v15, v129
	v_mov_b32_e32 v14, v129
	v_mov_b32_e32 v9, v129
	v_mov_b32_e32 v8, v129
	v_mov_b32_e32 v7, v129
	v_mov_b32_e32 v6, v129
	v_mov_b32_e32 v61, v129
	v_mov_b32_e32 v60, v129
	v_mov_b32_e32 v59, v129
	v_mov_b32_e32 v58, v129
	v_mov_b32_e32 v53, v129
	v_mov_b32_e32 v52, v129
	v_mov_b32_e32 v51, v129
	v_mov_b32_e32 v50, v129
	v_mov_b32_e32 v45, v129
	v_mov_b32_e32 v44, v129
	v_mov_b32_e32 v43, v129
	v_mov_b32_e32 v42, v129
	v_mov_b32_e32 v37, v129
	v_mov_b32_e32 v36, v129
	v_mov_b32_e32 v35, v129
	v_mov_b32_e32 v34, v129
	v_mov_b32_e32 v29, v129
	v_mov_b32_e32 v28, v129
	v_mov_b32_e32 v27, v129
	v_mov_b32_e32 v26, v129
	v_mov_b32_e32 v21, v129
	v_mov_b32_e32 v20, v129
	v_mov_b32_e32 v19, v129
	v_mov_b32_e32 v18, v129
	v_mov_b32_e32 v13, v129
	v_mov_b32_e32 v12, v129
	v_mov_b32_e32 v11, v129
	v_mov_b32_e32 v10, v129
	v_mov_b32_e32 v5, v129
	v_mov_b32_e32 v4, v129
	v_mov_b32_e32 v3, v129
	v_mov_b32_e32 v2, v129
.Lzs_1:
	s_cbranch_vccnz .LBB0_228
	s_and_b64 s[28:29], s[0:1], exec
	s_cselect_b32 s15, s19, s27
	s_cselect_b32 s17, s18, s26
	s_cselect_b32 s64, s21, s25
	s_cselect_b32 s65, s20, s24
	s_add_u32 s66, s24, 0x100
	s_addc_u32 s67, s25, 0
	s_add_u32 s24, s26, 0x40080
	s_addc_u32 s25, s27, 0
	s_mov_b32 s26, 0
	v_mov_b32_e32 v2, 0
	v_mov_b32_e32 v3, 0
	v_mov_b32_e32 v4, 0
	v_mov_b32_e32 v5, 0
	v_mov_b32_e32 v10, 0
	v_mov_b32_e32 v11, 0
	v_mov_b32_e32 v12, 0
	v_mov_b32_e32 v13, 0
	v_mov_b32_e32 v18, 0
	v_mov_b32_e32 v19, 0
	v_mov_b32_e32 v20, 0
	v_mov_b32_e32 v21, 0
	v_mov_b32_e32 v26, 0
	v_mov_b32_e32 v27, 0
	v_mov_b32_e32 v28, 0
	v_mov_b32_e32 v29, 0
	v_mov_b32_e32 v34, 0
	v_mov_b32_e32 v35, 0
	v_mov_b32_e32 v36, 0
	v_mov_b32_e32 v37, 0
	v_mov_b32_e32 v42, 0
	v_mov_b32_e32 v43, 0
	v_mov_b32_e32 v44, 0
	v_mov_b32_e32 v45, 0
	v_mov_b32_e32 v50, 0
	v_mov_b32_e32 v51, 0
	v_mov_b32_e32 v52, 0
	v_mov_b32_e32 v53, 0
	v_mov_b32_e32 v58, 0
	v_mov_b32_e32 v59, 0
	v_mov_b32_e32 v60, 0
	v_mov_b32_e32 v61, 0
	v_mov_b32_e32 v6, 0
	v_mov_b32_e32 v7, 0
	v_mov_b32_e32 v8, 0
	v_mov_b32_e32 v9, 0
	v_mov_b32_e32 v14, 0
	v_mov_b32_e32 v15, 0
	v_mov_b32_e32 v16, 0
	v_mov_b32_e32 v17, 0
	v_mov_b32_e32 v22, 0
	v_mov_b32_e32 v23, 0
	v_mov_b32_e32 v24, 0
	v_mov_b32_e32 v25, 0
	v_mov_b32_e32 v30, 0
	v_mov_b32_e32 v31, 0
	v_mov_b32_e32 v32, 0
	v_mov_b32_e32 v33, 0
	v_mov_b32_e32 v38, 0
	v_mov_b32_e32 v39, 0
	v_mov_b32_e32 v40, 0
	v_mov_b32_e32 v41, 0
	v_mov_b32_e32 v46, 0
	v_mov_b32_e32 v47, 0
	v_mov_b32_e32 v48, 0
	v_mov_b32_e32 v49, 0
	v_mov_b32_e32 v54, 0
	v_mov_b32_e32 v55, 0
	v_mov_b32_e32 v56, 0
	v_mov_b32_e32 v57, 0
	v_mov_b32_e32 v62, 0
	v_mov_b32_e32 v63, 0
	v_mov_b32_e32 v64, 0
	v_mov_b32_e32 v65, 0
	v_mov_b32_e32 v66, 0
	v_mov_b32_e32 v67, 0
	v_mov_b32_e32 v68, 0
	v_mov_b32_e32 v69, 0
	v_mov_b32_e32 v74, 0
	v_mov_b32_e32 v75, 0
	v_mov_b32_e32 v76, 0
	v_mov_b32_e32 v77, 0
	v_mov_b32_e32 v82, 0
	v_mov_b32_e32 v83, 0
	v_mov_b32_e32 v84, 0
	v_mov_b32_e32 v85, 0
	v_mov_b32_e32 v90, 0
	v_mov_b32_e32 v91, 0
	v_mov_b32_e32 v92, 0
	v_mov_b32_e32 v93, 0
	v_mov_b32_e32 v98, 0
	v_mov_b32_e32 v99, 0
	v_mov_b32_e32 v100, 0
	v_mov_b32_e32 v101, 0
	v_mov_b32_e32 v106, 0
	v_mov_b32_e32 v107, 0
	v_mov_b32_e32 v108, 0
	v_mov_b32_e32 v109, 0
	v_mov_b32_e32 v114, 0
	v_mov_b32_e32 v115, 0
	v_mov_b32_e32 v116, 0
	v_mov_b32_e32 v117, 0
	v_mov_b32_e32 v122, 0
	v_mov_b32_e32 v123, 0
	v_mov_b32_e32 v124, 0
	v_mov_b32_e32 v125, 0
	v_mov_b32_e32 v70, 0
	v_mov_b32_e32 v71, 0
	v_mov_b32_e32 v72, 0
	v_mov_b32_e32 v73, 0
	v_mov_b32_e32 v78, 0
	v_mov_b32_e32 v79, 0
	v_mov_b32_e32 v80, 0
	v_mov_b32_e32 v81, 0
	v_mov_b32_e32 v86, 0
	v_mov_b32_e32 v87, 0
	v_mov_b32_e32 v88, 0
	v_mov_b32_e32 v89, 0
	v_mov_b32_e32 v94, 0
	v_mov_b32_e32 v95, 0
	v_mov_b32_e32 v96, 0
	v_mov_b32_e32 v97, 0
	v_mov_b32_e32 v102, 0
	v_mov_b32_e32 v103, 0
	v_mov_b32_e32 v104, 0
	v_mov_b32_e32 v105, 0
	v_mov_b32_e32 v110, 0
	v_mov_b32_e32 v111, 0
	v_mov_b32_e32 v112, 0
	v_mov_b32_e32 v113, 0
	v_mov_b32_e32 v118, 0
	v_mov_b32_e32 v119, 0
	v_mov_b32_e32 v120, 0
	v_mov_b32_e32 v121, 0
	v_mov_b32_e32 v126, 0
	v_mov_b32_e32 v127, 0
	v_mov_b32_e32 v128, 0
	v_mov_b32_e32 v129, 0
	s_lshl_b32 s98, s63, 8
	s_ashr_i32 s99, s98, 31
	v_lshl_add_u64 v[242:243], s[98:99], 2, v[154:155]
	global_load_dwordx4 v[226:229], v[242:243], off
	global_load_dwordx4 v[230:233], v[242:243], off offset:512
	global_load_dwordx4 v[234:237], v[242:243], off offset:16
	global_load_dwordx4 v[238:241], v[242:243], off offset:528

;     __device__ bool next(int i, Unit& u) const { if (!b.next(i, u)) return false; const int seg = u.pn < 24 ? (u.pn >> 3) : u.pn - 21; u.pm += ((0x541320 >> (4 * seg)) & 7) * MROWS_TILES; return true; }
;     __device__ bool next(int i, Unit& u) const { if (!b.next(i, u)) return false; u.pm += (u.pn >> 3) * MROWS_TILES; return true; }
;     ...
;         const bool has_next = S.next(ui + 1, nxt);
;         const char* nA = has_next ? (const char*)g.A + (size_t)nxt.pm * tstepA : cA; const char* nB = has_next ? (const char*)g.Bt + (size_t)nxt.pn * tstepB : cB;
;     ...
; #pragma unroll
;         for (int a = 0; a < 2; ++a)
; #pragma unroll
;             for (int b = 0; b < 2; ++b)
; #pragma unroll
;                 for (int m = 0; m < 4; ++m)
; #pragma unroll
;                     for (int n = 0; n < 2; ++n) acc[a][b][m][n] = (f32x4){0.f, 0.f, 0.f, 0.f};
.LBB0_416:
	s_ashr_i32 s21, s20, 31
	s_lshl_b64 s[22:23], s[20:21], 20
	s_add_u32 s22, s35, s22
	s_addc_u32 s23, s36, s23
	s_ashr_i32 s19, s18, 31
	s_lshl_b64 s[24:25], s[18:19], 20
	s_add_u32 s24, s37, s24
	v_mov_b32_e32 v125, 0
	s_addc_u32 s25, s38, s25
	s_andn2_b64 vcc, exec, s[10:11]
	s_cbranch_vccz .Lzs_2
	v_mov_b32_e32 v124, v125
	v_mov_b32_e32 v123, v125
	v_mov_b32_e32 v122, v125
	v_mov_b32_e32 v129, v125
	v_mov_b32_e32 v128, v125
	v_mov_b32_e32 v127, v125
	v_mov_b32_e32 v126, v125
	v_mov_b32_e32 v113, v125
	v_mov_b32_e32 v112, v125
	v_mov_b32_e32 v111, v125
	v_mov_b32_e32 v110, v125
	v_mov_b32_e32 v109, v125
	v_mov_b32_e32 v108, v125
	v_mov_b32_e32 v107, v125
	v_mov_b32_e32 v106, v125
	v_mov_b32_e32 v97, v125
	v_mov_b32_e32 v96, v125
	v_mov_b32_e32 v95, v125
	v_mov_b32_e32 v94, v125
	v_mov_b32_e32 v93, v125
	v_mov_b32_e32 v92, v125
	v_mov_b32_e32 v91, v125
	v_mov_b32_e32 v90, v125
	v_mov_b32_e32 v81, v125
	v_mov_b32_e32 v80, v125
	v_mov_b32_e32 v79, v125
	v_mov_b32_e32 v78, v125
	v_mov_b32_e32 v77, v125
	v_mov_b32_e32 v76, v125
	v_mov_b32_e32 v75, v125
	v_mov_b32_e32 v74, v125
	v_mov_b32_e32 v121, v125
	v_mov_b32_e32 v120, v125
	v_mov_b32_e32 v119, v125
	v_mov_b32_e32 v118, v125
	v_mov_b32_e32 v117, v125
	v_mov_b32_e32 v116, v125
	v_mov_b32_e32 v115, v125
	v_mov_b32_e32 v114, v125
	v_mov_b32_e32 v105, v125
	v_mov_b32_e32 v104, v125
	v_mov_b32_e32 v103, v125
	v_mov_b32_e32 v102, v125
	v_mov_b32_e32 v101, v125
	v_mov_b32_e32 v100, v125
	v_mov_b32_e32 v99, v125
	v_mov_b32_e32 v98, v125
	v_mov_b32_e32 v89, v125
	v_mov_b32_e32 v88, v125
	v_mov_b32_e32 v87, v125
	v_mov_b32_e32 v86, v125
	v_mov_b32_e32 v85, v125
	v_mov_b32_e32 v84, v125
	v_mov_b32_e32 v83, v125
	v_mov_b32_e32 v82, v125
	v_mov_b32_e32 v73, v125
	v_mov_b32_e32 v72, v125
	v_mov_b32_e32 v71, v125
	v_mov_b32_e32 v70, v125
	v_mov_b32_e32 v69, v125
	v_mov_b32_e32 v68, v125
	v_mov_b32_e32 v67, v125
	v_mov_b32_e32 v66, v125
	v_mov_b32_e32 v65, v125
	v_mov_b32_e32 v64, v125
	v_mov_b32_e32 v63, v125
	v_mov_b32_e32 v62, v125
	v_mov_b32_e32 v61, v125
	v_mov_b32_e32 v60, v125
	v_mov_b32_e32 v59, v125
	v_mov_b32_e32 v58, v125
	v_mov_b32_e32 v49, v125
	v_mov_b32_e32 v48, v125
	v_mov_b32_e32 v47, v125
	v_mov_b32_e32 v46, v125
	v_mov_b32_e32 v45, v125
	v_mov_b32_e32 v44, v125
	v_mov_b32_e32 v43, v125
	v_mov_b32_e32 v42, v125
	v_mov_b32_e32 v33, v125
	v_mov_b32_e32 v32, v125
	v_mov_b32_e32 v31, v125
	v_mov_b32_e32 v30, v125
	v_mov_b32_e32 v29, v125
	v_mov_b32_e32 v28, v125
	v_mov_b32_e32 v27, v125
	v_mov_b32_e32 v26, v125
	v_mov_b32_e32 v17, v125
	v_mov_b32_e32 v16, v125
	v_mov_b32_e32 v15, v125
	v_mov_b32_e32 v14, v125
	v_mov_b32_e32 v13, v125
	v_mov_b32_e32 v12, v125
	v_mov_b32_e32 v11, v125
	v_mov_b32_e32 v10, v125
	v_mov_b32_e32 v57, v125
	v_mov_b32_e32 v56, v125
	v_mov_b32_e32 v55, v125
	v_mov_b32_e32 v54, v125
	v_mov_b32_e32 v53, v125
	v_mov_b32_e32 v52, v125
	v_mov_b32_e32 v51, v125
	v_mov_b32_e32 v50, v125
	v_mov_b32_e32 v41, v125
	v_mov_b32_e32 v40, v125
	v_mov_b32_e32 v39, v125
	v_mov_b32_e32 v38, v125
	v_mov_b32_e32 v37, v125
	v_mov_b32_e32 v36, v125
	v_mov_b32_e32 v35, v125
	v_mov_b32_e32 v34, v125
	v_mov_b32_e32 v25, v125
	v_mov_b32_e32 v24, v125
	v_mov_b32_e32 v23, v125
	v_mov_b32_e32 v22, v125
	v_mov_b32_e32 v21, v125
	v_mov_b32_e32 v20, v125
	v_mov_b32_e32 v19, v125
	v_mov_b32_e32 v18, v125
	v_mov_b32_e32 v9, v125
	v_mov_b32_e32 v8, v125
	v_mov_b32_e32 v7, v125
	v_mov_b32_e32 v6, v125
	v_mov_b32_e32 v5, v125
	v_mov_b32_e32 v4, v125
	v_mov_b32_e32 v3, v125
	v_mov_b32_e32 v2, v125
.Lzs_2:
	s_cbranch_vccnz .LBB0_419
	s_and_b64 s[30:31], s[0:1], exec
	s_cselect_b32 s19, s23, s29
	s_cselect_b32 s21, s22, s28
	s_cselect_b32 s61, s25, s27
	s_cselect_b32 s62, s24, s26
	s_add_u32 s63, s26, 0x100
	s_addc_u32 s64, s27, 0
	s_add_u32 s26, s28, 0x80080
	v_mov_b32_e32 v2, 0
	s_addc_u32 s27, s29, 0
	s_mov_b32 s28, 0
	v_mov_b32_e32 v3, v2
	v_mov_b32_e32 v4, v2
	v_mov_b32_e32 v5, v2
	v_mov_b32_e32 v6, v2
	v_mov_b32_e32 v7, v2
	v_mov_b32_e32 v8, v2
	v_mov_b32_e32 v9, v2
	v_mov_b32_e32 v18, v2
	v_mov_b32_e32 v19, v2
	v_mov_b32_e32 v20, v2
	v_mov_b32_e32 v21, v2
	v_mov_b32_e32 v22, v2
	v_mov_b32_e32 v23, v2
	v_mov_b32_e32 v24, v2
	v_mov_b32_e32 v25, v2
	v_mov_b32_e32 v34, v2
	v_mov_b32_e32 v35, v2
	v_mov_b32_e32 v36, v2
	v_mov_b32_e32 v37, v2
	v_mov_b32_e32 v38, v2
	v_mov_b32_e32 v39, v2
	v_mov_b32_e32 v40, v2
	v_mov_b32_e32 v41, v2
	v_mov_b32_e32 v50, v2
	v_mov_b32_e32 v51, v2
	v_mov_b32_e32 v52, v2
	v_mov_b32_e32 v53, v2
	v_mov_b32_e32 v54, v2
	v_mov_b32_e32 v55, v2
	v_mov_b32_e32 v56, v2
	v_mov_b32_e32 v57, v2
	v_mov_b32_e32 v10, v2
	v_mov_b32_e32 v11, v2
	v_mov_b32_e32 v12, v2
	v_mov_b32_e32 v13, v2
	v_mov_b32_e32 v14, v2
	v_mov_b32_e32 v15, v2
	v_mov_b32_e32 v16, v2
	v_mov_b32_e32 v17, v2
	v_mov_b32_e32 v26, v2
	v_mov_b32_e32 v27, v2
	v_mov_b32_e32 v28, v2
	v_mov_b32_e32 v29, v2
	v_mov_b32_e32 v30, v2
	v_mov_b32_e32 v31, v2
	v_mov_b32_e32 v32, v2
	v_mov_b32_e32 v33, v2
	v_mov_b32_e32 v42, v2
	v_mov_b32_e32 v43, v2
	v_mov_b32_e32 v44, v2
	v_mov_b32_e32 v45, v2
	v_mov_b32_e32 v46, v2
	v_mov_b32_e32 v47, v2
	v_mov_b32_e32 v48, v2
	v_mov_b32_e32 v49, v2
	v_mov_b32_e32 v58, v2
	v_mov_b32_e32 v59, v2
	v_mov_b32_e32 v60, v2
	v_mov_b32_e32 v61, v2
	v_mov_b32_e32 v62, v2
	v_mov_b32_e32 v63, v2
	v_mov_b32_e32 v64, v2
	v_mov_b32_e32 v65, v2
	v_mov_b32_e32 v66, v2
	v_mov_b32_e32 v67, v2
	v_mov_b32_e32 v68, v2
	v_mov_b32_e32 v69, v2
	v_mov_b32_e32 v70, v2
	v_mov_b32_e32 v71, v2
	v_mov_b32_e32 v72, v2
	v_mov_b32_e32 v73, v2
	v_mov_b32_e32 v82, v2
	v_mov_b32_e32 v83, v2
	v_mov_b32_e32 v84, v2
	v_mov_b32_e32 v85, v2
	v_mov_b32_e32 v86, v2
	v_mov_b32_e32 v87, v2
	v_mov_b32_e32 v88, v2
	v_mov_b32_e32 v89, v2
	v_mov_b32_e32 v98, v2
	v_mov_b32_e32 v99, v2
	v_mov_b32_e32 v100, v2
	v_mov_b32_e32 v101, v2
	v_mov_b32_e32 v102, v2
	v_mov_b32_e32 v103, v2
	v_mov_b32_e32 v104, v2
	v_mov_b32_e32 v105, v2
	v_mov_b32_e32 v114, v2
	v_mov_b32_e32 v115, v2
	v_mov_b32_e32 v116, v2
	v_mov_b32_e32 v117, v2
	v_mov_b32_e32 v118, v2
	v_mov_b32_e32 v119, v2
	v_mov_b32_e32 v120, v2
	v_mov_b32_e32 v121, v2
	v_mov_b32_e32 v74, v2
	v_mov_b32_e32 v75, v2
	v_mov_b32_e32 v76, v2
	v_mov_b32_e32 v77, v2
	v_mov_b32_e32 v78, v2
	v_mov_b32_e32 v79, v2
	v_mov_b32_e32 v80, v2
	v_mov_b32_e32 v81, v2
	v_mov_b32_e32 v90, v2
	v_mov_b32_e32 v91, v2
	v_mov_b32_e32 v92, v2
	v_mov_b32_e32 v93, v2
	v_mov_b32_e32 v94, v2
	v_mov_b32_e32 v95, v2
	v_mov_b32_e32 v96, v2
	v_mov_b32_e32 v97, v2
	v_mov_b32_e32 v106, v2
	v_mov_b32_e32 v107, v2
	v_mov_b32_e32 v108, v2
	v_mov_b32_e32 v109, v2
	v_mov_b32_e32 v110, v2
	v_mov_b32_e32 v111, v2
	v_mov_b32_e32 v112, v2
	v_mov_b32_e32 v113, v2
	v_mov_b32_e32 v126, v2
	v_mov_b32_e32 v127, v2
	v_mov_b32_e32 v128, v2
	v_mov_b32_e32 v129, v2
	v_mov_b32_e32 v122, v2
	v_mov_b32_e32 v123, v2
	v_mov_b32_e32 v124, v2
	v_mov_b32_e32 v125, v2

;     __device__ bool next(int i, Unit& u) const { if (!b.next(i, u)) return false; const int seg = u.pn < 24 ? (u.pn >> 3) : u.pn - 21; u.pm += ((0x541320 >> (4 * seg)) & 7) * MROWS_TILES; return true; }
;     __device__ bool next(int i, Unit& u) const { if (!b.next(i, u)) return false; u.pm += (u.pn >> 3) * MROWS_TILES; return true; }
;     ...
;         const bool has_next = S.next(ui + 1, nxt);
;         const char* nA = has_next ? (const char*)g.A + (size_t)nxt.pm * tstepA : cA; const char* nB = has_next ? (const char*)g.Bt + (size_t)nxt.pn * tstepB : cB;
;     ...
; #pragma unroll
;         for (int a = 0; a < 2; ++a)
; #pragma unroll
;             for (int b = 0; b < 2; ++b)
; #pragma unroll
;                 for (int m = 0; m < 4; ++m)
; #pragma unroll
;                     for (int n = 0; n < 2; ++n) acc[a][b][m][n] = (f32x4){0.f, 0.f, 0.f, 0.f};
.LBB0_711:
	s_ashr_i32 s25, s24, 31
	s_lshl_b64 s[26:27], s[24:25], 20
	s_add_u32 s26, s42, s26
	s_addc_u32 s27, s43, s27
	s_ashr_i32 s23, s22, 31
	s_lshl_b64 s[28:29], s[22:23], 20
	s_add_u32 s28, s44, s28
	v_mov_b32_e32 v125, 0
	s_addc_u32 s29, s45, s29
	s_andn2_b64 vcc, exec, s[12:13]
	s_cbranch_vccz .Lzs_3
	v_mov_b32_e32 v124, v125
	v_mov_b32_e32 v123, v125
	v_mov_b32_e32 v122, v125
	v_mov_b32_e32 v129, v125
	v_mov_b32_e32 v128, v125
	v_mov_b32_e32 v127, v125
	v_mov_b32_e32 v126, v125
	v_mov_b32_e32 v113, v125
	v_mov_b32_e32 v112, v125
	v_mov_b32_e32 v111, v125
	v_mov_b32_e32 v110, v125
	v_mov_b32_e32 v109, v125
	v_mov_b32_e32 v108, v125
	v_mov_b32_e32 v107, v125
	v_mov_b32_e32 v106, v125
	v_mov_b32_e32 v97, v125
	v_mov_b32_e32 v96, v125
	v_mov_b32_e32 v95, v125
	v_mov_b32_e32 v94, v125
	v_mov_b32_e32 v93, v125
	v_mov_b32_e32 v92, v125
	v_mov_b32_e32 v91, v125
	v_mov_b32_e32 v90, v125
	v_mov_b32_e32 v81, v125
	v_mov_b32_e32 v80, v125
	v_mov_b32_e32 v79, v125
	v_mov_b32_e32 v78, v125
	v_mov_b32_e32 v77, v125
	v_mov_b32_e32 v76, v125
	v_mov_b32_e32 v75, v125
	v_mov_b32_e32 v74, v125
	v_mov_b32_e32 v121, v125
	v_mov_b32_e32 v120, v125
	v_mov_b32_e32 v119, v125
	v_mov_b32_e32 v118, v125
	v_mov_b32_e32 v117, v125
	v_mov_b32_e32 v116, v125
	v_mov_b32_e32 v115, v125
	v_mov_b32_e32 v114, v125
	v_mov_b32_e32 v105, v125
	v_mov_b32_e32 v104, v125
	v_mov_b32_e32 v103, v125
	v_mov_b32_e32 v102, v125
	v_mov_b32_e32 v101, v125
	v_mov_b32_e32 v100, v125
	v_mov_b32_e32 v99, v125
	v_mov_b32_e32 v98, v125
	v_mov_b32_e32 v89, v125
	v_mov_b32_e32 v88, v125
	v_mov_b32_e32 v87, v125
	v_mov_b32_e32 v86, v125
	v_mov_b32_e32 v85, v125
	v_mov_b32_e32 v84, v125
	v_mov_b32_e32 v83, v125
	v_mov_b32_e32 v82, v125
	v_mov_b32_e32 v73, v125
	v_mov_b32_e32 v72, v125
	v_mov_b32_e32 v71, v125
	v_mov_b32_e32 v70, v125
	v_mov_b32_e32 v69, v125
	v_mov_b32_e32 v68, v125
	v_mov_b32_e32 v67, v125
	v_mov_b32_e32 v66, v125
	v_mov_b32_e32 v65, v125
	v_mov_b32_e32 v64, v125
	v_mov_b32_e32 v63, v125
	v_mov_b32_e32 v62, v125
	v_mov_b32_e32 v61, v125
	v_mov_b32_e32 v60, v125
	v_mov_b32_e32 v59, v125
	v_mov_b32_e32 v58, v125
	v_mov_b32_e32 v49, v125
	v_mov_b32_e32 v48, v125
	v_mov_b32_e32 v47, v125
	v_mov_b32_e32 v46, v125
	v_mov_b32_e32 v45, v125
	v_mov_b32_e32 v44, v125
	v_mov_b32_e32 v43, v125
	v_mov_b32_e32 v42, v125
	v_mov_b32_e32 v33, v125
	v_mov_b32_e32 v32, v125
	v_mov_b32_e32 v31, v125
	v_mov_b32_e32 v30, v125
	v_mov_b32_e32 v29, v125
	v_mov_b32_e32 v28, v125
	v_mov_b32_e32 v27, v125
	v_mov_b32_e32 v26, v125
	v_mov_b32_e32 v17, v125
	v_mov_b32_e32 v16, v125
	v_mov_b32_e32 v15, v125
	v_mov_b32_e32 v14, v125
	v_mov_b32_e32 v13, v125
	v_mov_b32_e32 v12, v125
	v_mov_b32_e32 v11, v125
	v_mov_b32_e32 v10, v125
	v_mov_b32_e32 v57, v125
	v_mov_b32_e32 v56, v125
	v_mov_b32_e32 v55, v125
	v_mov_b32_e32 v54, v125
	v_mov_b32_e32 v53, v125
	v_mov_b32_e32 v52, v125
	v_mov_b32_e32 v51, v125
	v_mov_b32_e32 v50, v125
	v_mov_b32_e32 v41, v125
	v_mov_b32_e32 v40, v125
	v_mov_b32_e32 v39, v125
	v_mov_b32_e32 v38, v125
	v_mov_b32_e32 v37, v125
	v_mov_b32_e32 v36, v125
	v_mov_b32_e32 v35, v125
	v_mov_b32_e32 v34, v125
	v_mov_b32_e32 v25, v125
	v_mov_b32_e32 v24, v125
	v_mov_b32_e32 v23, v125
	v_mov_b32_e32 v22, v125
	v_mov_b32_e32 v21, v125
	v_mov_b32_e32 v20, v125
	v_mov_b32_e32 v19, v125
	v_mov_b32_e32 v18, v125
	v_mov_b32_e32 v9, v125
	v_mov_b32_e32 v8, v125
	v_mov_b32_e32 v7, v125
	v_mov_b32_e32 v6, v125
	v_mov_b32_e32 v5, v125
	v_mov_b32_e32 v4, v125
	v_mov_b32_e32 v3, v125
	v_mov_b32_e32 v2, v125
.Lzs_3:
	s_cbranch_vccnz .LBB0_714
	s_and_b64 s[38:39], s[0:1], exec
	s_cselect_b32 s23, s27, s37
	s_cselect_b32 s25, s26, s36
	s_cselect_b32 s65, s29, s35
	s_cselect_b32 s66, s28, s34
	s_add_u32 s67, s34, 0x100
	s_addc_u32 s68, s35, 0
	s_add_u32 s34, s36, 0x80080
	v_mov_b32_e32 v2, 0
	s_addc_u32 s35, s37, 0
	s_mov_b32 s36, 0
	v_mov_b32_e32 v3, v2
	v_mov_b32_e32 v4, v2
	v_mov_b32_e32 v5, v2
	v_mov_b32_e32 v6, v2
	v_mov_b32_e32 v7, v2
	v_mov_b32_e32 v8, v2
	v_mov_b32_e32 v9, v2
	v_mov_b32_e32 v18, v2
	v_mov_b32_e32 v19, v2
	v_mov_b32_e32 v20, v2
	v_mov_b32_e32 v21, v2
	v_mov_b32_e32 v22, v2
	v_mov_b32_e32 v23, v2
	v_mov_b32_e32 v24, v2
	v_mov_b32_e32 v25, v2
	v_mov_b32_e32 v34, v2
	v_mov_b32_e32 v35, v2
	v_mov_b32_e32 v36, v2
	v_mov_b32_e32 v37, v2
	v_mov_b32_e32 v38, v2
	v_mov_b32_e32 v39, v2
	v_mov_b32_e32 v40, v2
	v_mov_b32_e32 v41, v2
	v_mov_b32_e32 v50, v2
	v_mov_b32_e32 v51, v2
	v_mov_b32_e32 v52, v2
	v_mov_b32_e32 v53, v2
	v_mov_b32_e32 v54, v2
	v_mov_b32_e32 v55, v2
	v_mov_b32_e32 v56, v2
	v_mov_b32_e32 v57, v2
	v_mov_b32_e32 v10, v2
	v_mov_b32_e32 v11, v2
	v_mov_b32_e32 v12, v2
	v_mov_b32_e32 v13, v2
	v_mov_b32_e32 v14, v2
	v_mov_b32_e32 v15, v2
	v_mov_b32_e32 v16, v2
	v_mov_b32_e32 v17, v2
	v_mov_b32_e32 v26, v2
	v_mov_b32_e32 v27, v2
	v_mov_b32_e32 v28, v2
	v_mov_b32_e32 v29, v2
	v_mov_b32_e32 v30, v2
	v_mov_b32_e32 v31, v2
	v_mov_b32_e32 v32, v2
	v_mov_b32_e32 v33, v2
	v_mov_b32_e32 v42, v2
	v_mov_b32_e32 v43, v2
	v_mov_b32_e32 v44, v2
	v_mov_b32_e32 v45, v2
	v_mov_b32_e32 v46, v2
	v_mov_b32_e32 v47, v2
	v_mov_b32_e32 v48, v2
	v_mov_b32_e32 v49, v2
	v_mov_b32_e32 v58, v2
	v_mov_b32_e32 v59, v2
	v_mov_b32_e32 v60, v2
	v_mov_b32_e32 v61, v2
	v_mov_b32_e32 v62, v2
	v_mov_b32_e32 v63, v2
	v_mov_b32_e32 v64, v2
	v_mov_b32_e32 v65, v2
	v_mov_b32_e32 v66, v2
	v_mov_b32_e32 v67, v2
	v_mov_b32_e32 v68, v2
	v_mov_b32_e32 v69, v2
	v_mov_b32_e32 v70, v2
	v_mov_b32_e32 v71, v2
	v_mov_b32_e32 v72, v2
	v_mov_b32_e32 v73, v2
	v_mov_b32_e32 v82, v2
	v_mov_b32_e32 v83, v2
	v_mov_b32_e32 v84, v2
	v_mov_b32_e32 v85, v2
	v_mov_b32_e32 v86, v2
	v_mov_b32_e32 v87, v2
	v_mov_b32_e32 v88, v2
	v_mov_b32_e32 v89, v2
	v_mov_b32_e32 v98, v2
	v_mov_b32_e32 v99, v2
	v_mov_b32_e32 v100, v2
	v_mov_b32_e32 v101, v2
	v_mov_b32_e32 v102, v2
	v_mov_b32_e32 v103, v2
	v_mov_b32_e32 v104, v2
	v_mov_b32_e32 v105, v2
	v_mov_b32_e32 v114, v2
	v_mov_b32_e32 v115, v2
	v_mov_b32_e32 v116, v2
	v_mov_b32_e32 v117, v2
	v_mov_b32_e32 v118, v2
	v_mov_b32_e32 v119, v2
	v_mov_b32_e32 v120, v2
	v_mov_b32_e32 v121, v2
	v_mov_b32_e32 v74, v2
	v_mov_b32_e32 v75, v2
	v_mov_b32_e32 v76, v2
	v_mov_b32_e32 v77, v2
	v_mov_b32_e32 v78, v2
	v_mov_b32_e32 v79, v2
	v_mov_b32_e32 v80, v2
	v_mov_b32_e32 v81, v2
	v_mov_b32_e32 v90, v2
	v_mov_b32_e32 v91, v2
	v_mov_b32_e32 v92, v2
	v_mov_b32_e32 v93, v2
	v_mov_b32_e32 v94, v2
	v_mov_b32_e32 v95, v2
	v_mov_b32_e32 v96, v2
	v_mov_b32_e32 v97, v2
	v_mov_b32_e32 v106, v2
	v_mov_b32_e32 v107, v2
	v_mov_b32_e32 v108, v2
	v_mov_b32_e32 v109, v2
	v_mov_b32_e32 v110, v2
	v_mov_b32_e32 v111, v2
	v_mov_b32_e32 v112, v2
	v_mov_b32_e32 v113, v2
	v_mov_b32_e32 v126, v2
	v_mov_b32_e32 v127, v2
	v_mov_b32_e32 v128, v2
	v_mov_b32_e32 v129, v2
	v_mov_b32_e32 v122, v2
	v_mov_b32_e32 v123, v2
	v_mov_b32_e32 v124, v2
	v_mov_b32_e32 v125, v2

;     __device__ bool next(int i, Unit& u) const { if (!b.next(i, u)) return false; const int seg = u.pn < 24 ? (u.pn >> 3) : u.pn - 21; u.pm += ((0x541320 >> (4 * seg)) & 7) * MROWS_TILES; return true; }
;     __device__ bool next(int i, Unit& u) const { if (!b.next(i, u)) return false; u.pm += (u.pn >> 3) * MROWS_TILES; return true; }
;     ...
;         const bool has_next = S.next(ui + 1, nxt);
;         const char* nA = has_next ? (const char*)g.A + (size_t)nxt.pm * tstepA : cA; const char* nB = has_next ? (const char*)g.Bt + (size_t)nxt.pn * tstepB : cB;
;     ...
; #pragma unroll
;         for (int a = 0; a < 2; ++a)
; #pragma unroll
;             for (int b = 0; b < 2; ++b)
; #pragma unroll
;                 for (int m = 0; m < 4; ++m)
; #pragma unroll
;                     for (int n = 0; n < 2; ++n) acc[a][b][m][n] = (f32x4){0.f, 0.f, 0.f, 0.f};
.LBB0_2260:
	s_ashr_i32 s17, s16, 31
	s_lshl_b64 s[18:19], s[16:17], 20
	s_add_u32 s18, s36, s18
	s_addc_u32 s19, s37, s19
	s_ashr_i32 s15, s14, 31
	s_lshl_b64 s[20:21], s[14:15], 20
	s_add_u32 s20, s38, s20
	v_mov_b32_e32 v129, 0
	s_addc_u32 s21, s39, s21
	s_andn2_b64 vcc, exec, s[10:11]
	s_cbranch_vccz .Lzs_9
	v_mov_b32_e32 v128, v129
	v_mov_b32_e32 v127, v129
	v_mov_b32_e32 v126, v129
	v_mov_b32_e32 v125, v129
	v_mov_b32_e32 v124, v129
	v_mov_b32_e32 v123, v129
	v_mov_b32_e32 v122, v129
	v_mov_b32_e32 v113, v129
	v_mov_b32_e32 v112, v129
	v_mov_b32_e32 v111, v129
	v_mov_b32_e32 v110, v129
	v_mov_b32_e32 v109, v129
	v_mov_b32_e32 v108, v129
	v_mov_b32_e32 v107, v129
	v_mov_b32_e32 v106, v129
	v_mov_b32_e32 v97, v129
	v_mov_b32_e32 v96, v129
	v_mov_b32_e32 v95, v129
	v_mov_b32_e32 v94, v129
	v_mov_b32_e32 v93, v129
	v_mov_b32_e32 v92, v129
	v_mov_b32_e32 v91, v129
	v_mov_b32_e32 v90, v129
	v_mov_b32_e32 v81, v129
	v_mov_b32_e32 v80, v129
	v_mov_b32_e32 v79, v129
	v_mov_b32_e32 v78, v129
	v_mov_b32_e32 v77, v129
	v_mov_b32_e32 v76, v129
	v_mov_b32_e32 v75, v129
	v_mov_b32_e32 v74, v129
	v_mov_b32_e32 v121, v129
	v_mov_b32_e32 v120, v129
	v_mov_b32_e32 v119, v129
	v_mov_b32_e32 v118, v129
	v_mov_b32_e32 v117, v129
	v_mov_b32_e32 v116, v129
	v_mov_b32_e32 v115, v129
	v_mov_b32_e32 v114, v129
	v_mov_b32_e32 v105, v129
	v_mov_b32_e32 v104, v129
	v_mov_b32_e32 v103, v129
	v_mov_b32_e32 v102, v129
	v_mov_b32_e32 v101, v129
	v_mov_b32_e32 v100, v129
	v_mov_b32_e32 v99, v129
	v_mov_b32_e32 v98, v129
	v_mov_b32_e32 v89, v129
	v_mov_b32_e32 v88, v129
	v_mov_b32_e32 v87, v129
	v_mov_b32_e32 v86, v129
	v_mov_b32_e32 v85, v129
	v_mov_b32_e32 v84, v129
	v_mov_b32_e32 v83, v129
	v_mov_b32_e32 v82, v129
	v_mov_b32_e32 v73, v129
	v_mov_b32_e32 v72, v129
	v_mov_b32_e32 v71, v129
	v_mov_b32_e32 v70, v129
	v_mov_b32_e32 v69, v129
	v_mov_b32_e32 v68, v129
	v_mov_b32_e32 v67, v129
	v_mov_b32_e32 v66, v129
	v_mov_b32_e32 v65, v129
	v_mov_b32_e32 v64, v129
	v_mov_b32_e32 v63, v129
	v_mov_b32_e32 v62, v129
	v_mov_b32_e32 v61, v129
	v_mov_b32_e32 v60, v129
	v_mov_b32_e32 v59, v129
	v_mov_b32_e32 v58, v129
	v_mov_b32_e32 v49, v129
	v_mov_b32_e32 v48, v129
	v_mov_b32_e32 v47, v129
	v_mov_b32_e32 v46, v129
	v_mov_b32_e32 v45, v129
	v_mov_b32_e32 v44, v129
	v_mov_b32_e32 v43, v129
	v_mov_b32_e32 v42, v129
	v_mov_b32_e32 v33, v129
	v_mov_b32_e32 v32, v129
	v_mov_b32_e32 v31, v129
	v_mov_b32_e32 v30, v129
	v_mov_b32_e32 v29, v129
	v_mov_b32_e32 v28, v129
	v_mov_b32_e32 v27, v129
	v_mov_b32_e32 v26, v129
	v_mov_b32_e32 v17, v129
	v_mov_b32_e32 v16, v129
	v_mov_b32_e32 v15, v129
	v_mov_b32_e32 v14, v129
	v_mov_b32_e32 v13, v129
	v_mov_b32_e32 v12, v129
	v_mov_b32_e32 v11, v129
	v_mov_b32_e32 v10, v129
	v_mov_b32_e32 v57, v129
	v_mov_b32_e32 v56, v129
	v_mov_b32_e32 v55, v129
	v_mov_b32_e32 v54, v129
	v_mov_b32_e32 v53, v129
	v_mov_b32_e32 v52, v129
	v_mov_b32_e32 v51, v129
	v_mov_b32_e32 v50, v129
	v_mov_b32_e32 v41, v129
	v_mov_b32_e32 v40, v129
	v_mov_b32_e32 v39, v129
	v_mov_b32_e32 v38, v129
	v_mov_b32_e32 v37, v129
	v_mov_b32_e32 v36, v129
	v_mov_b32_e32 v35, v129
	v_mov_b32_e32 v34, v129
	v_mov_b32_e32 v25, v129
	v_mov_b32_e32 v24, v129
	v_mov_b32_e32 v23, v129
	v_mov_b32_e32 v22, v129
	v_mov_b32_e32 v21, v129
	v_mov_b32_e32 v20, v129
	v_mov_b32_e32 v19, v129
	v_mov_b32_e32 v18, v129
	v_mov_b32_e32 v9, v129
	v_mov_b32_e32 v8, v129
	v_mov_b32_e32 v7, v129
	v_mov_b32_e32 v6, v129
	v_mov_b32_e32 v5, v129
	v_mov_b32_e32 v4, v129
	v_mov_b32_e32 v3, v129
	v_mov_b32_e32 v2, v129
.Lzs_9:
	s_cbranch_vccnz .LBB0_2263
	s_and_b64 s[30:31], s[4:5], exec
	s_cselect_b32 s2, s19, s29
	s_cselect_b32 s15, s18, s28
	s_cselect_b32 s17, s21, s27
	s_cselect_b32 s23, s20, s26
	s_add_u32 s25, s26, 0x100
	s_addc_u32 s64, s27, 0
	s_add_u32 s26, s28, 0x80080
	v_mov_b32_e32 v2, 0
	s_addc_u32 s27, s29, 0
	s_mov_b32 s28, 0
	v_mov_b32_e32 v3, v2
	v_mov_b32_e32 v4, v2
	v_mov_b32_e32 v5, v2
	v_mov_b32_e32 v6, v2
	v_mov_b32_e32 v7, v2
	v_mov_b32_e32 v8, v2
	v_mov_b32_e32 v9, v2
	v_mov_b32_e32 v18, v2
	v_mov_b32_e32 v19, v2
	v_mov_b32_e32 v20, v2
	v_mov_b32_e32 v21, v2
	v_mov_b32_e32 v22, v2
	v_mov_b32_e32 v23, v2
	v_mov_b32_e32 v24, v2
	v_mov_b32_e32 v25, v2
	v_mov_b32_e32 v34, v2
	v_mov_b32_e32 v35, v2
	v_mov_b32_e32 v36, v2
	v_mov_b32_e32 v37, v2
	v_mov_b32_e32 v38, v2
	v_mov_b32_e32 v39, v2
	v_mov_b32_e32 v40, v2
	v_mov_b32_e32 v41, v2
	v_mov_b32_e32 v50, v2
	v_mov_b32_e32 v51, v2
	v_mov_b32_e32 v52, v2
	v_mov_b32_e32 v53, v2
	v_mov_b32_e32 v54, v2
	v_mov_b32_e32 v55, v2
	v_mov_b32_e32 v56, v2
	v_mov_b32_e32 v57, v2
	v_mov_b32_e32 v10, v2
	v_mov_b32_e32 v11, v2
	v_mov_b32_e32 v12, v2
	v_mov_b32_e32 v13, v2
	v_mov_b32_e32 v14, v2
	v_mov_b32_e32 v15, v2
	v_mov_b32_e32 v16, v2
	v_mov_b32_e32 v17, v2
	v_mov_b32_e32 v26, v2
	v_mov_b32_e32 v27, v2
	v_mov_b32_e32 v28, v2
	v_mov_b32_e32 v29, v2
	v_mov_b32_e32 v30, v2
	v_mov_b32_e32 v31, v2
	v_mov_b32_e32 v32, v2
	v_mov_b32_e32 v33, v2
	v_mov_b32_e32 v42, v2
	v_mov_b32_e32 v43, v2
	v_mov_b32_e32 v44, v2
	v_mov_b32_e32 v45, v2
	v_mov_b32_e32 v46, v2
	v_mov_b32_e32 v47, v2
	v_mov_b32_e32 v48, v2
	v_mov_b32_e32 v49, v2
	v_mov_b32_e32 v58, v2
	v_mov_b32_e32 v59, v2
	v_mov_b32_e32 v60, v2
	v_mov_b32_e32 v61, v2
	v_mov_b32_e32 v62, v2
	v_mov_b32_e32 v63, v2
	v_mov_b32_e32 v64, v2
	v_mov_b32_e32 v65, v2
	v_mov_b32_e32 v66, v2
	v_mov_b32_e32 v67, v2
	v_mov_b32_e32 v68, v2
	v_mov_b32_e32 v69, v2
	v_mov_b32_e32 v70, v2
	v_mov_b32_e32 v71, v2
	v_mov_b32_e32 v72, v2
	v_mov_b32_e32 v73, v2
	v_mov_b32_e32 v82, v2
	v_mov_b32_e32 v83, v2
	v_mov_b32_e32 v84, v2
	v_mov_b32_e32 v85, v2
	v_mov_b32_e32 v86, v2
	v_mov_b32_e32 v87, v2
	v_mov_b32_e32 v88, v2
	v_mov_b32_e32 v89, v2
	v_mov_b32_e32 v98, v2
	v_mov_b32_e32 v99, v2
	v_mov_b32_e32 v100, v2
	v_mov_b32_e32 v101, v2
	v_mov_b32_e32 v102, v2
	v_mov_b32_e32 v103, v2
	v_mov_b32_e32 v104, v2
	v_mov_b32_e32 v105, v2
	v_mov_b32_e32 v114, v2
	v_mov_b32_e32 v115, v2
	v_mov_b32_e32 v116, v2
	v_mov_b32_e32 v117, v2
	v_mov_b32_e32 v118, v2
	v_mov_b32_e32 v119, v2
	v_mov_b32_e32 v120, v2
	v_mov_b32_e32 v121, v2
	v_mov_b32_e32 v74, v2
	v_mov_b32_e32 v75, v2
	v_mov_b32_e32 v76, v2
	v_mov_b32_e32 v77, v2
	v_mov_b32_e32 v78, v2
	v_mov_b32_e32 v79, v2
	v_mov_b32_e32 v80, v2
	v_mov_b32_e32 v81, v2
	v_mov_b32_e32 v90, v2
	v_mov_b32_e32 v91, v2
	v_mov_b32_e32 v92, v2
	v_mov_b32_e32 v93, v2
	v_mov_b32_e32 v94, v2
	v_mov_b32_e32 v95, v2
	v_mov_b32_e32 v96, v2
	v_mov_b32_e32 v97, v2
	v_mov_b32_e32 v106, v2
	v_mov_b32_e32 v107, v2
	v_mov_b32_e32 v108, v2
	v_mov_b32_e32 v109, v2
	v_mov_b32_e32 v110, v2
	v_mov_b32_e32 v111, v2
	v_mov_b32_e32 v112, v2
	v_mov_b32_e32 v113, v2
	v_mov_b32_e32 v122, v2
	v_mov_b32_e32 v123, v2
	v_mov_b32_e32 v124, v2
	v_mov_b32_e32 v125, v2
	v_mov_b32_e32 v126, v2
	v_mov_b32_e32 v127, v2
	v_mov_b32_e32 v128, v2
	v_mov_b32_e32 v129, v2

;     ...
;         const char* nA = has_next ? (const char*)g.A + (size_t)nxt.pm * tstepA : cA; const char* nB = has_next ? (const char*)g.Bt + (size_t)nxt.pn * tstepB : cB;
;         for (int t = 0; t < nt; t += 2) {
;     ...
; #pragma unroll
;         for (int a = 0; a < 2; ++a)
; #pragma unroll
;             for (int b = 0; b < 2; ++b)
; #pragma unroll
;                 for (int m = 0; m < 4; ++m)
; #pragma unroll
;                     for (int n = 0; n < 2; ++n) acc[a][b][m][n] = (f32x4){0.f, 0.f, 0.f, 0.f};
.LBB0_3354:
	s_ashr_i32 s31, s30, 31
	s_lshl_b64 s[34:35], s[30:31], 17
	s_add_u32 s34, s48, s34
	s_addc_u32 s35, s49, s35
	s_ashr_i32 s29, s28, 31
	s_lshl_b64 s[36:37], s[28:29], 17
	s_add_u32 s36, s50, s36
	v_mov_b32_e32 v129, 0
	s_addc_u32 s37, s51, s37
	s_andn2_b64 vcc, exec, s[16:17]
	s_cbranch_vccz .Lzs_10
	v_mov_b32_e32 v128, v129
	v_mov_b32_e32 v127, v129
	v_mov_b32_e32 v126, v129
	v_mov_b32_e32 v125, v129
	v_mov_b32_e32 v124, v129
	v_mov_b32_e32 v123, v129
	v_mov_b32_e32 v122, v129
	v_mov_b32_e32 v113, v129
	v_mov_b32_e32 v112, v129
	v_mov_b32_e32 v111, v129
	v_mov_b32_e32 v110, v129
	v_mov_b32_e32 v109, v129
	v_mov_b32_e32 v108, v129
	v_mov_b32_e32 v107, v129
	v_mov_b32_e32 v106, v129
	v_mov_b32_e32 v97, v129
	v_mov_b32_e32 v96, v129
	v_mov_b32_e32 v95, v129
	v_mov_b32_e32 v94, v129
	v_mov_b32_e32 v93, v129
	v_mov_b32_e32 v92, v129
	v_mov_b32_e32 v91, v129
	v_mov_b32_e32 v90, v129
	v_mov_b32_e32 v81, v129
	v_mov_b32_e32 v80, v129
	v_mov_b32_e32 v79, v129
	v_mov_b32_e32 v78, v129
	v_mov_b32_e32 v77, v129
	v_mov_b32_e32 v76, v129
	v_mov_b32_e32 v75, v129
	v_mov_b32_e32 v74, v129
	v_mov_b32_e32 v121, v129
	v_mov_b32_e32 v120, v129
	v_mov_b32_e32 v119, v129
	v_mov_b32_e32 v118, v129
	v_mov_b32_e32 v117, v129
	v_mov_b32_e32 v116, v129
	v_mov_b32_e32 v115, v129
	v_mov_b32_e32 v114, v129
	v_mov_b32_e32 v105, v129
	v_mov_b32_e32 v104, v129
	v_mov_b32_e32 v103, v129
	v_mov_b32_e32 v102, v129
	v_mov_b32_e32 v101, v129
	v_mov_b32_e32 v100, v129
	v_mov_b32_e32 v99, v129
	v_mov_b32_e32 v98, v129
	v_mov_b32_e32 v89, v129
	v_mov_b32_e32 v88, v129
	v_mov_b32_e32 v87, v129
	v_mov_b32_e32 v86, v129
	v_mov_b32_e32 v85, v129
	v_mov_b32_e32 v84, v129
	v_mov_b32_e32 v83, v129
	v_mov_b32_e32 v82, v129
	v_mov_b32_e32 v73, v129
	v_mov_b32_e32 v72, v129
	v_mov_b32_e32 v71, v129
	v_mov_b32_e32 v70, v129
	v_mov_b32_e32 v69, v129
	v_mov_b32_e32 v68, v129
	v_mov_b32_e32 v67, v129
	v_mov_b32_e32 v66, v129
	v_mov_b32_e32 v65, v129
	v_mov_b32_e32 v64, v129
	v_mov_b32_e32 v63, v129
	v_mov_b32_e32 v62, v129
	v_mov_b32_e32 v61, v129
	v_mov_b32_e32 v60, v129
	v_mov_b32_e32 v59, v129
	v_mov_b32_e32 v58, v129
	v_mov_b32_e32 v49, v129
	v_mov_b32_e32 v48, v129
	v_mov_b32_e32 v47, v129
	v_mov_b32_e32 v46, v129
	v_mov_b32_e32 v45, v129
	v_mov_b32_e32 v44, v129
	v_mov_b32_e32 v43, v129
	v_mov_b32_e32 v42, v129
	v_mov_b32_e32 v33, v129
	v_mov_b32_e32 v32, v129
	v_mov_b32_e32 v31, v129
	v_mov_b32_e32 v30, v129
	v_mov_b32_e32 v29, v129
	v_mov_b32_e32 v28, v129
	v_mov_b32_e32 v27, v129
	v_mov_b32_e32 v26, v129
	v_mov_b32_e32 v17, v129
	v_mov_b32_e32 v16, v129
	v_mov_b32_e32 v15, v129
	v_mov_b32_e32 v14, v129
	v_mov_b32_e32 v13, v129
	v_mov_b32_e32 v12, v129
	v_mov_b32_e32 v11, v129
	v_mov_b32_e32 v10, v129
	v_mov_b32_e32 v57, v129
	v_mov_b32_e32 v56, v129
	v_mov_b32_e32 v55, v129
	v_mov_b32_e32 v54, v129
	v_mov_b32_e32 v53, v129
	v_mov_b32_e32 v52, v129
	v_mov_b32_e32 v51, v129
	v_mov_b32_e32 v50, v129
	v_mov_b32_e32 v41, v129
	v_mov_b32_e32 v40, v129
	v_mov_b32_e32 v39, v129
	v_mov_b32_e32 v38, v129
	v_mov_b32_e32 v37, v129
	v_mov_b32_e32 v36, v129
	v_mov_b32_e32 v35, v129
	v_mov_b32_e32 v34, v129
	v_mov_b32_e32 v25, v129
	v_mov_b32_e32 v24, v129
	v_mov_b32_e32 v23, v129
	v_mov_b32_e32 v22, v129
	v_mov_b32_e32 v21, v129
	v_mov_b32_e32 v20, v129
	v_mov_b32_e32 v19, v129
	v_mov_b32_e32 v18, v129
	v_mov_b32_e32 v9, v129
	v_mov_b32_e32 v8, v129
	v_mov_b32_e32 v7, v129
	v_mov_b32_e32 v6, v129
	v_mov_b32_e32 v5, v129
	v_mov_b32_e32 v4, v129
	v_mov_b32_e32 v3, v129
	v_mov_b32_e32 v2, v129
.Lzs_10:
	s_cbranch_vccnz .LBB0_3358
	s_and_b64 s[44:45], s[0:1], exec
	s_cselect_b32 s3, s35, s43
	s_cselect_b32 s29, s34, s42
	s_cselect_b32 s31, s37, s41
	s_cselect_b32 s39, s36, s40
	s_add_u32 s76, s40, 0x100
	s_addc_u32 s77, s41, 0
	s_add_u32 s40, s42, 0x10080
	v_mov_b32_e32 v2, 0
	s_addc_u32 s41, s43, 0
	s_mov_b32 s42, 0
	v_mov_b32_e32 v3, v2
	v_mov_b32_e32 v4, v2
	v_mov_b32_e32 v5, v2
	v_mov_b32_e32 v6, v2
	v_mov_b32_e32 v7, v2
	v_mov_b32_e32 v8, v2
	v_mov_b32_e32 v9, v2
	v_mov_b32_e32 v18, v2
	v_mov_b32_e32 v19, v2
	v_mov_b32_e32 v20, v2
	v_mov_b32_e32 v21, v2
	v_mov_b32_e32 v22, v2
	v_mov_b32_e32 v23, v2
	v_mov_b32_e32 v24, v2
	v_mov_b32_e32 v25, v2
	v_mov_b32_e32 v34, v2
	v_mov_b32_e32 v35, v2
	v_mov_b32_e32 v36, v2
	v_mov_b32_e32 v37, v2
	v_mov_b32_e32 v38, v2
	v_mov_b32_e32 v39, v2
	v_mov_b32_e32 v40, v2
	v_mov_b32_e32 v41, v2
	v_mov_b32_e32 v50, v2
	v_mov_b32_e32 v51, v2
	v_mov_b32_e32 v52, v2
	v_mov_b32_e32 v53, v2
	v_mov_b32_e32 v54, v2
	v_mov_b32_e32 v55, v2
	v_mov_b32_e32 v56, v2
	v_mov_b32_e32 v57, v2
	v_mov_b32_e32 v10, v2
	v_mov_b32_e32 v11, v2
	v_mov_b32_e32 v12, v2
	v_mov_b32_e32 v13, v2
	v_mov_b32_e32 v14, v2
	v_mov_b32_e32 v15, v2
	v_mov_b32_e32 v16, v2
	v_mov_b32_e32 v17, v2
	v_mov_b32_e32 v26, v2
	v_mov_b32_e32 v27, v2
	v_mov_b32_e32 v28, v2
	v_mov_b32_e32 v29, v2
	v_mov_b32_e32 v30, v2
	v_mov_b32_e32 v31, v2
	v_mov_b32_e32 v32, v2
	v_mov_b32_e32 v33, v2
	v_mov_b32_e32 v42, v2
	v_mov_b32_e32 v43, v2
	v_mov_b32_e32 v44, v2
	v_mov_b32_e32 v45, v2
	v_mov_b32_e32 v46, v2
	v_mov_b32_e32 v47, v2
	v_mov_b32_e32 v48, v2
	v_mov_b32_e32 v49, v2
	v_mov_b32_e32 v58, v2
	v_mov_b32_e32 v59, v2
	v_mov_b32_e32 v60, v2
	v_mov_b32_e32 v61, v2
	v_mov_b32_e32 v62, v2
	v_mov_b32_e32 v63, v2
	v_mov_b32_e32 v64, v2
	v_mov_b32_e32 v65, v2
	v_mov_b32_e32 v66, v2
	v_mov_b32_e32 v67, v2
	v_mov_b32_e32 v68, v2
	v_mov_b32_e32 v69, v2
	v_mov_b32_e32 v70, v2
	v_mov_b32_e32 v71, v2
	v_mov_b32_e32 v72, v2
	v_mov_b32_e32 v73, v2
	v_mov_b32_e32 v82, v2
	v_mov_b32_e32 v83, v2
	v_mov_b32_e32 v84, v2
	v_mov_b32_e32 v85, v2
	v_mov_b32_e32 v86, v2
	v_mov_b32_e32 v87, v2
	v_mov_b32_e32 v88, v2
	v_mov_b32_e32 v89, v2
	v_mov_b32_e32 v98, v2
	v_mov_b32_e32 v99, v2
	v_mov_b32_e32 v100, v2
	v_mov_b32_e32 v101, v2
	v_mov_b32_e32 v102, v2
	v_mov_b32_e32 v103, v2
	v_mov_b32_e32 v104, v2
	v_mov_b32_e32 v105, v2
	v_mov_b32_e32 v114, v2
	v_mov_b32_e32 v115, v2
	v_mov_b32_e32 v116, v2
	v_mov_b32_e32 v117, v2
	v_mov_b32_e32 v118, v2
	v_mov_b32_e32 v119, v2
	v_mov_b32_e32 v120, v2
	v_mov_b32_e32 v121, v2
	v_mov_b32_e32 v74, v2
	v_mov_b32_e32 v75, v2
	v_mov_b32_e32 v76, v2
	v_mov_b32_e32 v77, v2
	v_mov_b32_e32 v78, v2
	v_mov_b32_e32 v79, v2
	v_mov_b32_e32 v80, v2
	v_mov_b32_e32 v81, v2
	v_mov_b32_e32 v90, v2
	v_mov_b32_e32 v91, v2
	v_mov_b32_e32 v92, v2
	v_mov_b32_e32 v93, v2
	v_mov_b32_e32 v94, v2
	v_mov_b32_e32 v95, v2
	v_mov_b32_e32 v96, v2
	v_mov_b32_e32 v97, v2
	v_mov_b32_e32 v106, v2
	v_mov_b32_e32 v107, v2
	v_mov_b32_e32 v108, v2
	v_mov_b32_e32 v109, v2
	v_mov_b32_e32 v110, v2
	v_mov_b32_e32 v111, v2
	v_mov_b32_e32 v112, v2
	v_mov_b32_e32 v113, v2
	v_mov_b32_e32 v122, v2
	v_mov_b32_e32 v123, v2
	v_mov_b32_e32 v124, v2
	v_mov_b32_e32 v125, v2
	v_mov_b32_e32 v126, v2
	v_mov_b32_e32 v127, v2
	v_mov_b32_e32 v128, v2
	v_mov_b32_e32 v129, v2

;     ...
;         const char* nA = has_next ? (const char*)g.A + (size_t)nxt.pm * tstepA : cA; const char* nB = has_next ? (const char*)g.Bt + (size_t)nxt.pn * tstepB : cB;
;         for (int t = 0; t < nt; t += 2) {
;     ...
; #pragma unroll
;         for (int a = 0; a < 2; ++a)
; #pragma unroll
;             for (int b = 0; b < 2; ++b)
; #pragma unroll
;                 for (int m = 0; m < 4; ++m)
; #pragma unroll
;                     for (int n = 0; n < 2; ++n) acc[a][b][m][n] = (f32x4){0.f, 0.f, 0.f, 0.f};
.LBB0_4139:
	s_ashr_i32 s17, s16, 31
	s_lshl_b64 s[18:19], s[16:17], 19
	s_add_u32 s18, s37, s18
	s_addc_u32 s19, s38, s19
	s_ashr_i32 s15, s14, 31
	s_lshl_b64 s[20:21], s[14:15], 19
	s_add_u32 s20, s39, s20
	v_mov_b32_e32 v137, 0
	s_addc_u32 s21, s40, s21
	s_andn2_b64 vcc, exec, s[10:11]
	s_cbranch_vccz .Lzs_13
	v_mov_b32_e32 v136, v137
	v_mov_b32_e32 v135, v137
	v_mov_b32_e32 v134, v137
	v_mov_b32_e32 v117, v137
	v_mov_b32_e32 v116, v137
	v_mov_b32_e32 v115, v137
	v_mov_b32_e32 v114, v137
	v_mov_b32_e32 v109, v137
	v_mov_b32_e32 v108, v137
	v_mov_b32_e32 v107, v137
	v_mov_b32_e32 v106, v137
	v_mov_b32_e32 v101, v137
	v_mov_b32_e32 v100, v137
	v_mov_b32_e32 v99, v137
	v_mov_b32_e32 v98, v137
	v_mov_b32_e32 v93, v137
	v_mov_b32_e32 v92, v137
	v_mov_b32_e32 v91, v137
	v_mov_b32_e32 v90, v137
	v_mov_b32_e32 v85, v137
	v_mov_b32_e32 v84, v137
	v_mov_b32_e32 v83, v137
	v_mov_b32_e32 v82, v137
	v_mov_b32_e32 v77, v137
	v_mov_b32_e32 v76, v137
	v_mov_b32_e32 v75, v137
	v_mov_b32_e32 v74, v137
	v_mov_b32_e32 v69, v137
	v_mov_b32_e32 v68, v137
	v_mov_b32_e32 v67, v137
	v_mov_b32_e32 v66, v137
	v_mov_b32_e32 v141, v137
	v_mov_b32_e32 v140, v137
	v_mov_b32_e32 v139, v137
	v_mov_b32_e32 v138, v137
	v_mov_b32_e32 v121, v137
	v_mov_b32_e32 v120, v137
	v_mov_b32_e32 v119, v137
	v_mov_b32_e32 v118, v137
	v_mov_b32_e32 v113, v137
	v_mov_b32_e32 v112, v137
	v_mov_b32_e32 v111, v137
	v_mov_b32_e32 v110, v137
	v_mov_b32_e32 v105, v137
	v_mov_b32_e32 v104, v137
	v_mov_b32_e32 v103, v137
	v_mov_b32_e32 v102, v137
	v_mov_b32_e32 v97, v137
	v_mov_b32_e32 v96, v137
	v_mov_b32_e32 v95, v137
	v_mov_b32_e32 v94, v137
	v_mov_b32_e32 v89, v137
	v_mov_b32_e32 v88, v137
	v_mov_b32_e32 v87, v137
	v_mov_b32_e32 v86, v137
	v_mov_b32_e32 v81, v137
	v_mov_b32_e32 v80, v137
	v_mov_b32_e32 v79, v137
	v_mov_b32_e32 v78, v137
	v_mov_b32_e32 v73, v137
	v_mov_b32_e32 v72, v137
	v_mov_b32_e32 v71, v137
	v_mov_b32_e32 v70, v137
	v_mov_b32_e32 v61, v137
	v_mov_b32_e32 v60, v137
	v_mov_b32_e32 v59, v137
	v_mov_b32_e32 v58, v137
	v_mov_b32_e32 v53, v137
	v_mov_b32_e32 v52, v137
	v_mov_b32_e32 v51, v137
	v_mov_b32_e32 v50, v137
	v_mov_b32_e32 v45, v137
	v_mov_b32_e32 v44, v137
	v_mov_b32_e32 v43, v137
	v_mov_b32_e32 v42, v137
	v_mov_b32_e32 v37, v137
	v_mov_b32_e32 v36, v137
	v_mov_b32_e32 v35, v137
	v_mov_b32_e32 v34, v137
	v_mov_b32_e32 v29, v137
	v_mov_b32_e32 v28, v137
	v_mov_b32_e32 v27, v137
	v_mov_b32_e32 v26, v137
	v_mov_b32_e32 v21, v137
	v_mov_b32_e32 v20, v137
	v_mov_b32_e32 v19, v137
	v_mov_b32_e32 v18, v137
	v_mov_b32_e32 v13, v137
	v_mov_b32_e32 v12, v137
	v_mov_b32_e32 v11, v137
	v_mov_b32_e32 v10, v137
	v_mov_b32_e32 v5, v137
	v_mov_b32_e32 v4, v137
	v_mov_b32_e32 v3, v137
	v_mov_b32_e32 v2, v137
	v_mov_b32_e32 v65, v137
	v_mov_b32_e32 v64, v137
	v_mov_b32_e32 v63, v137
	v_mov_b32_e32 v62, v137
	v_mov_b32_e32 v57, v137
	v_mov_b32_e32 v56, v137
	v_mov_b32_e32 v55, v137
	v_mov_b32_e32 v54, v137
	v_mov_b32_e32 v49, v137
	v_mov_b32_e32 v48, v137
	v_mov_b32_e32 v47, v137
	v_mov_b32_e32 v46, v137
	v_mov_b32_e32 v41, v137
	v_mov_b32_e32 v40, v137
	v_mov_b32_e32 v39, v137
	v_mov_b32_e32 v38, v137
	v_mov_b32_e32 v33, v137
	v_mov_b32_e32 v32, v137
	v_mov_b32_e32 v31, v137
	v_mov_b32_e32 v30, v137
	v_mov_b32_e32 v25, v137
	v_mov_b32_e32 v24, v137
	v_mov_b32_e32 v23, v137
	v_mov_b32_e32 v22, v137
	v_mov_b32_e32 v17, v137
	v_mov_b32_e32 v16, v137
	v_mov_b32_e32 v15, v137
	v_mov_b32_e32 v14, v137
	v_mov_b32_e32 v9, v137
	v_mov_b32_e32 v8, v137
	v_mov_b32_e32 v7, v137
	v_mov_b32_e32 v6, v137
.Lzs_13:
	s_cbranch_vccnz .LBB0_4142
	s_and_b64 s[28:29], s[0:1], exec
	s_cselect_b32 s15, s19, s27
	s_cselect_b32 s17, s18, s26
	s_cselect_b32 s65, s21, s25
	s_cselect_b32 s66, s20, s24
	s_add_u32 s67, s24, 0x100
	s_addc_u32 s68, s25, 0
	s_add_u32 s24, s26, 0x40080
	s_addc_u32 s25, s27, 0
	s_mov_b32 s26, 0
	v_mov_b32_e32 v6, 0
	v_mov_b32_e32 v7, 0
	v_mov_b32_e32 v8, 0
	v_mov_b32_e32 v9, 0
	v_mov_b32_e32 v14, 0
	v_mov_b32_e32 v15, 0
	v_mov_b32_e32 v16, 0
	v_mov_b32_e32 v17, 0
	v_mov_b32_e32 v22, 0
	v_mov_b32_e32 v23, 0
	v_mov_b32_e32 v24, 0
	v_mov_b32_e32 v25, 0
	v_mov_b32_e32 v30, 0
	v_mov_b32_e32 v31, 0
	v_mov_b32_e32 v32, 0
	v_mov_b32_e32 v33, 0
	v_mov_b32_e32 v38, 0
	v_mov_b32_e32 v39, 0
	v_mov_b32_e32 v40, 0
	v_mov_b32_e32 v41, 0
	v_mov_b32_e32 v46, 0
	v_mov_b32_e32 v47, 0
	v_mov_b32_e32 v48, 0
	v_mov_b32_e32 v49, 0
	v_mov_b32_e32 v54, 0
	v_mov_b32_e32 v55, 0
	v_mov_b32_e32 v56, 0
	v_mov_b32_e32 v57, 0
	v_mov_b32_e32 v62, 0
	v_mov_b32_e32 v63, 0
	v_mov_b32_e32 v64, 0
	v_mov_b32_e32 v65, 0
	v_mov_b32_e32 v2, 0
	v_mov_b32_e32 v3, 0
	v_mov_b32_e32 v4, 0
	v_mov_b32_e32 v5, 0
	v_mov_b32_e32 v10, 0
	v_mov_b32_e32 v11, 0
	v_mov_b32_e32 v12, 0
	v_mov_b32_e32 v13, 0
	v_mov_b32_e32 v18, 0
	v_mov_b32_e32 v19, 0
	v_mov_b32_e32 v20, 0
	v_mov_b32_e32 v21, 0
	v_mov_b32_e32 v26, 0
	v_mov_b32_e32 v27, 0
	v_mov_b32_e32 v28, 0
	v_mov_b32_e32 v29, 0
	v_mov_b32_e32 v34, 0
	v_mov_b32_e32 v35, 0
	v_mov_b32_e32 v36, 0
	v_mov_b32_e32 v37, 0
	v_mov_b32_e32 v42, 0
	v_mov_b32_e32 v43, 0
	v_mov_b32_e32 v44, 0
	v_mov_b32_e32 v45, 0
	v_mov_b32_e32 v50, 0
	v_mov_b32_e32 v51, 0
	v_mov_b32_e32 v52, 0
	v_mov_b32_e32 v53, 0
	v_mov_b32_e32 v58, 0
	v_mov_b32_e32 v59, 0
	v_mov_b32_e32 v60, 0
	v_mov_b32_e32 v61, 0
	v_mov_b32_e32 v70, 0
	v_mov_b32_e32 v71, 0
	v_mov_b32_e32 v72, 0
	v_mov_b32_e32 v73, 0
	v_mov_b32_e32 v78, 0
	v_mov_b32_e32 v79, 0
	v_mov_b32_e32 v80, 0
	v_mov_b32_e32 v81, 0
	v_mov_b32_e32 v86, 0
	v_mov_b32_e32 v87, 0
	v_mov_b32_e32 v88, 0
	v_mov_b32_e32 v89, 0
	v_mov_b32_e32 v94, 0
	v_mov_b32_e32 v95, 0
	v_mov_b32_e32 v96, 0
	v_mov_b32_e32 v97, 0
	v_mov_b32_e32 v102, 0
	v_mov_b32_e32 v103, 0
	v_mov_b32_e32 v104, 0
	v_mov_b32_e32 v105, 0
	v_mov_b32_e32 v110, 0
	v_mov_b32_e32 v111, 0
	v_mov_b32_e32 v112, 0
	v_mov_b32_e32 v113, 0
	v_mov_b32_e32 v118, 0
	v_mov_b32_e32 v119, 0
	v_mov_b32_e32 v120, 0
	v_mov_b32_e32 v121, 0
	v_mov_b32_e32 v138, 0
	v_mov_b32_e32 v139, 0
	v_mov_b32_e32 v140, 0
	v_mov_b32_e32 v141, 0
	v_mov_b32_e32 v66, 0
	v_mov_b32_e32 v67, 0
	v_mov_b32_e32 v68, 0
	v_mov_b32_e32 v69, 0
	v_mov_b32_e32 v74, 0
	v_mov_b32_e32 v75, 0
	v_mov_b32_e32 v76, 0
	v_mov_b32_e32 v77, 0
	v_mov_b32_e32 v82, 0
	v_mov_b32_e32 v83, 0
	v_mov_b32_e32 v84, 0
	v_mov_b32_e32 v85, 0
	v_mov_b32_e32 v90, 0
	v_mov_b32_e32 v91, 0
	v_mov_b32_e32 v92, 0
	v_mov_b32_e32 v93, 0
	v_mov_b32_e32 v98, 0
	v_mov_b32_e32 v99, 0
	v_mov_b32_e32 v100, 0
	v_mov_b32_e32 v101, 0
	v_mov_b32_e32 v106, 0
	v_mov_b32_e32 v107, 0
	v_mov_b32_e32 v108, 0
	v_mov_b32_e32 v109, 0
	v_mov_b32_e32 v114, 0
	v_mov_b32_e32 v115, 0
	v_mov_b32_e32 v116, 0
	v_mov_b32_e32 v117, 0
	v_mov_b32_e32 v134, 0
	v_mov_b32_e32 v135, 0
	v_mov_b32_e32 v136, 0
	v_mov_b32_e32 v137, 0

;     ...
;         for (int t = 0; t < nt; t += 2) {
;     ...
; #pragma unroll
;         for (int a = 0; a < 2; ++a)
; #pragma unroll
;             for (int b = 0; b < 2; ++b)
; #pragma unroll
;                 for (int m = 0; m < 4; ++m)
; #pragma unroll
;                     for (int n = 0; n < 2; ++n) acc[a][b][m][n] = (f32x4){0.f, 0.f, 0.f, 0.f};
.LBB0_4215:
	v_mov_b32_e32 v113, 0
	s_andn2_b64 vcc, exec, s[14:15]
	s_cbranch_vccz .Lzs_14
	v_mov_b32_e32 v112, v113
	v_mov_b32_e32 v111, v113
	v_mov_b32_e32 v110, v113
	v_mov_b32_e32 v121, v113
	v_mov_b32_e32 v120, v113
	v_mov_b32_e32 v119, v113
	v_mov_b32_e32 v118, v113
	v_mov_b32_e32 v125, v113
	v_mov_b32_e32 v124, v113
	v_mov_b32_e32 v123, v113
	v_mov_b32_e32 v122, v113
	v_mov_b32_e32 v129, v113
	v_mov_b32_e32 v128, v113
	v_mov_b32_e32 v127, v113
	v_mov_b32_e32 v126, v113
	v_mov_b32_e32 v149, v113
	v_mov_b32_e32 v148, v113
	v_mov_b32_e32 v147, v113
	v_mov_b32_e32 v146, v113
	v_mov_b32_e32 v153, v113
	v_mov_b32_e32 v152, v113
	v_mov_b32_e32 v151, v113
	v_mov_b32_e32 v150, v113
	v_mov_b32_e32 v157, v113
	v_mov_b32_e32 v156, v113
	v_mov_b32_e32 v155, v113
	v_mov_b32_e32 v154, v113
	v_mov_b32_e32 v161, v113
	v_mov_b32_e32 v160, v113
	v_mov_b32_e32 v159, v113
	v_mov_b32_e32 v158, v113
	v_mov_b32_e32 v101, v113
	v_mov_b32_e32 v100, v113
	v_mov_b32_e32 v99, v113
	v_mov_b32_e32 v98, v113
	v_mov_b32_e32 v105, v113
	v_mov_b32_e32 v104, v113
	v_mov_b32_e32 v103, v113
	v_mov_b32_e32 v102, v113
	v_mov_b32_e32 v109, v113
	v_mov_b32_e32 v108, v113
	v_mov_b32_e32 v107, v113
	v_mov_b32_e32 v106, v113
	v_mov_b32_e32 v117, v113
	v_mov_b32_e32 v116, v113
	v_mov_b32_e32 v115, v113
	v_mov_b32_e32 v114, v113
	v_mov_b32_e32 v133, v113
	v_mov_b32_e32 v132, v113
	v_mov_b32_e32 v131, v113
	v_mov_b32_e32 v130, v113
	v_mov_b32_e32 v137, v113
	v_mov_b32_e32 v136, v113
	v_mov_b32_e32 v135, v113
	v_mov_b32_e32 v134, v113
	v_mov_b32_e32 v141, v113
	v_mov_b32_e32 v140, v113
	v_mov_b32_e32 v139, v113
	v_mov_b32_e32 v138, v113
	v_mov_b32_e32 v145, v113
	v_mov_b32_e32 v144, v113
	v_mov_b32_e32 v143, v113
	v_mov_b32_e32 v142, v113
	v_mov_b32_e32 v45, v113
	v_mov_b32_e32 v44, v113
	v_mov_b32_e32 v43, v113
	v_mov_b32_e32 v42, v113
	v_mov_b32_e32 v49, v113
	v_mov_b32_e32 v48, v113
	v_mov_b32_e32 v47, v113
	v_mov_b32_e32 v46, v113
	v_mov_b32_e32 v61, v113
	v_mov_b32_e32 v60, v113
	v_mov_b32_e32 v59, v113
	v_mov_b32_e32 v58, v113
	v_mov_b32_e32 v65, v113
	v_mov_b32_e32 v64, v113
	v_mov_b32_e32 v63, v113
	v_mov_b32_e32 v62, v113
	v_mov_b32_e32 v77, v113
	v_mov_b32_e32 v76, v113
	v_mov_b32_e32 v75, v113
	v_mov_b32_e32 v74, v113
	v_mov_b32_e32 v81, v113
	v_mov_b32_e32 v80, v113
	v_mov_b32_e32 v79, v113
	v_mov_b32_e32 v78, v113
	v_mov_b32_e32 v93, v113
	v_mov_b32_e32 v92, v113
	v_mov_b32_e32 v91, v113
	v_mov_b32_e32 v90, v113
	v_mov_b32_e32 v97, v113
	v_mov_b32_e32 v96, v113
	v_mov_b32_e32 v95, v113
	v_mov_b32_e32 v94, v113
	v_mov_b32_e32 v37, v113
	v_mov_b32_e32 v36, v113
	v_mov_b32_e32 v35, v113
	v_mov_b32_e32 v34, v113
	v_mov_b32_e32 v41, v113
	v_mov_b32_e32 v40, v113
	v_mov_b32_e32 v39, v113
	v_mov_b32_e32 v38, v113
	v_mov_b32_e32 v53, v113
	v_mov_b32_e32 v52, v113
	v_mov_b32_e32 v51, v113
	v_mov_b32_e32 v50, v113
	v_mov_b32_e32 v57, v113
	v_mov_b32_e32 v56, v113
	v_mov_b32_e32 v55, v113
	v_mov_b32_e32 v54, v113
	v_mov_b32_e32 v69, v113
	v_mov_b32_e32 v68, v113
	v_mov_b32_e32 v67, v113
	v_mov_b32_e32 v66, v113
	v_mov_b32_e32 v73, v113
	v_mov_b32_e32 v72, v113
	v_mov_b32_e32 v71, v113
	v_mov_b32_e32 v70, v113
	v_mov_b32_e32 v85, v113
	v_mov_b32_e32 v84, v113
	v_mov_b32_e32 v83, v113
	v_mov_b32_e32 v82, v113
	v_mov_b32_e32 v89, v113
	v_mov_b32_e32 v88, v113
	v_mov_b32_e32 v87, v113
	v_mov_b32_e32 v86, v113
.Lzs_14:
	s_cbranch_vccnz .LBB0_4218
	s_add_u32 s66, s30, 0x100
	v_mov_b32_e32 v86, 0
	s_addc_u32 s67, s31, 0
	s_mov_b32 s34, 0
	v_mov_b32_e32 v87, v86
	v_mov_b32_e32 v88, v86
	v_mov_b32_e32 v89, v86
	v_mov_b32_e32 v82, v86
	v_mov_b32_e32 v83, v86
	v_mov_b32_e32 v84, v86
	v_mov_b32_e32 v85, v86
	v_mov_b32_e32 v70, v86
	v_mov_b32_e32 v71, v86
	v_mov_b32_e32 v72, v86
	v_mov_b32_e32 v73, v86
	v_mov_b32_e32 v66, v86
	v_mov_b32_e32 v67, v86
	v_mov_b32_e32 v68, v86
	v_mov_b32_e32 v69, v86
	v_mov_b32_e32 v54, v86
	v_mov_b32_e32 v55, v86
	v_mov_b32_e32 v56, v86
	v_mov_b32_e32 v57, v86
	v_mov_b32_e32 v50, v86
	v_mov_b32_e32 v51, v86
	v_mov_b32_e32 v52, v86
	v_mov_b32_e32 v53, v86
	v_mov_b32_e32 v38, v86
	v_mov_b32_e32 v39, v86
	v_mov_b32_e32 v40, v86
	v_mov_b32_e32 v41, v86
	v_mov_b32_e32 v34, v86
	v_mov_b32_e32 v35, v86
	v_mov_b32_e32 v36, v86
	v_mov_b32_e32 v37, v86
	v_mov_b32_e32 v94, v86
	v_mov_b32_e32 v95, v86
	v_mov_b32_e32 v96, v86
	v_mov_b32_e32 v97, v86
	v_mov_b32_e32 v90, v86
	v_mov_b32_e32 v91, v86
	v_mov_b32_e32 v92, v86
	v_mov_b32_e32 v93, v86
	v_mov_b32_e32 v78, v86
	v_mov_b32_e32 v79, v86
	v_mov_b32_e32 v80, v86
	v_mov_b32_e32 v81, v86
	v_mov_b32_e32 v74, v86
	v_mov_b32_e32 v75, v86
	v_mov_b32_e32 v76, v86
	v_mov_b32_e32 v77, v86
	v_mov_b32_e32 v62, v86
	v_mov_b32_e32 v63, v86
	v_mov_b32_e32 v64, v86
	v_mov_b32_e32 v65, v86
	v_mov_b32_e32 v58, v86
	v_mov_b32_e32 v59, v86
	v_mov_b32_e32 v60, v86
	v_mov_b32_e32 v61, v86
	v_mov_b32_e32 v46, v86
	v_mov_b32_e32 v47, v86
	v_mov_b32_e32 v48, v86
	v_mov_b32_e32 v49, v86
	v_mov_b32_e32 v42, v86
	v_mov_b32_e32 v43, v86
	v_mov_b32_e32 v44, v86
	v_mov_b32_e32 v45, v86
	v_mov_b32_e32 v142, v86
	v_mov_b32_e32 v143, v86
	v_mov_b32_e32 v144, v86
	v_mov_b32_e32 v145, v86
	v_mov_b32_e32 v138, v86
	v_mov_b32_e32 v139, v86
	v_mov_b32_e32 v140, v86
	v_mov_b32_e32 v141, v86
	v_mov_b32_e32 v134, v86
	v_mov_b32_e32 v135, v86
	v_mov_b32_e32 v136, v86
	v_mov_b32_e32 v137, v86
	v_mov_b32_e32 v130, v86
	v_mov_b32_e32 v131, v86
	v_mov_b32_e32 v132, v86
	v_mov_b32_e32 v133, v86
	v_mov_b32_e32 v114, v86
	v_mov_b32_e32 v115, v86
	v_mov_b32_e32 v116, v86
	v_mov_b32_e32 v117, v86
	v_mov_b32_e32 v106, v86
	v_mov_b32_e32 v107, v86
	v_mov_b32_e32 v108, v86
	v_mov_b32_e32 v109, v86
	v_mov_b32_e32 v102, v86
	v_mov_b32_e32 v103, v86
	v_mov_b32_e32 v104, v86
	v_mov_b32_e32 v105, v86
	v_mov_b32_e32 v98, v86
	v_mov_b32_e32 v99, v86
	v_mov_b32_e32 v100, v86
	v_mov_b32_e32 v101, v86
	v_mov_b32_e32 v158, v86
	v_mov_b32_e32 v159, v86
	v_mov_b32_e32 v160, v86
	v_mov_b32_e32 v161, v86
	v_mov_b32_e32 v154, v86
	v_mov_b32_e32 v155, v86
	v_mov_b32_e32 v156, v86
	v_mov_b32_e32 v157, v86
	v_mov_b32_e32 v150, v86
	v_mov_b32_e32 v151, v86
	v_mov_b32_e32 v152, v86
	v_mov_b32_e32 v153, v86
	v_mov_b32_e32 v146, v86
	v_mov_b32_e32 v147, v86
	v_mov_b32_e32 v148, v86
	v_mov_b32_e32 v149, v86
	v_mov_b32_e32 v126, v86
	v_mov_b32_e32 v127, v86
	v_mov_b32_e32 v128, v86
	v_mov_b32_e32 v129, v86
	v_mov_b32_e32 v122, v86
	v_mov_b32_e32 v123, v86
	v_mov_b32_e32 v124, v86
	v_mov_b32_e32 v125, v86
	v_mov_b32_e32 v118, v86
	v_mov_b32_e32 v119, v86
	v_mov_b32_e32 v120, v86
	v_mov_b32_e32 v121, v86
	v_mov_b32_e32 v110, v86
	v_mov_b32_e32 v111, v86
	v_mov_b32_e32 v112, v86
	v_mov_b32_e32 v113, v86

;     ...
;         const char* nA = has_next ? (const char*)g.A + (size_t)nxt.pm * tstepA : cA; const char* nB = has_next ? (const char*)g.Bt + (size_t)nxt.pn * tstepB : cB;
;         for (int t = 0; t < nt; t += 2) {
;     ...
; #pragma unroll
;         for (int a = 0; a < 2; ++a)
; #pragma unroll
;             for (int b = 0; b < 2; ++b)
; #pragma unroll
;                 for (int m = 0; m < 4; ++m)
; #pragma unroll
;                     for (int n = 0; n < 2; ++n) acc[a][b][m][n] = (f32x4){0.f, 0.f, 0.f, 0.f};
.LBB0_4644:
	s_ashr_i32 s27, s26, 31
	s_lshl_b64 s[28:29], s[26:27], 20
	s_add_u32 s28, s44, s28
	s_addc_u32 s29, s45, s29
	s_ashr_i32 s25, s24, 31
	s_lshl_b64 s[30:31], s[24:25], 20
	s_add_u32 s30, s46, s30
	v_mov_b32_e32 v125, 0
	s_addc_u32 s31, s47, s31
	s_andn2_b64 vcc, exec, s[14:15]
	s_cbranch_vccz .Lzs_15
	v_mov_b32_e32 v124, v125
	v_mov_b32_e32 v123, v125
	v_mov_b32_e32 v122, v125
	v_mov_b32_e32 v129, v125
	v_mov_b32_e32 v128, v125
	v_mov_b32_e32 v127, v125
	v_mov_b32_e32 v126, v125
	v_mov_b32_e32 v113, v125
	v_mov_b32_e32 v112, v125
	v_mov_b32_e32 v111, v125
	v_mov_b32_e32 v110, v125
	v_mov_b32_e32 v109, v125
	v_mov_b32_e32 v108, v125
	v_mov_b32_e32 v107, v125
	v_mov_b32_e32 v106, v125
	v_mov_b32_e32 v97, v125
	v_mov_b32_e32 v96, v125
	v_mov_b32_e32 v95, v125
	v_mov_b32_e32 v94, v125
	v_mov_b32_e32 v93, v125
	v_mov_b32_e32 v92, v125
	v_mov_b32_e32 v91, v125
	v_mov_b32_e32 v90, v125
	v_mov_b32_e32 v81, v125
	v_mov_b32_e32 v80, v125
	v_mov_b32_e32 v79, v125
	v_mov_b32_e32 v78, v125
	v_mov_b32_e32 v77, v125
	v_mov_b32_e32 v76, v125
	v_mov_b32_e32 v75, v125
	v_mov_b32_e32 v74, v125
	v_mov_b32_e32 v121, v125
	v_mov_b32_e32 v120, v125
	v_mov_b32_e32 v119, v125
	v_mov_b32_e32 v118, v125
	v_mov_b32_e32 v117, v125
	v_mov_b32_e32 v116, v125
	v_mov_b32_e32 v115, v125
	v_mov_b32_e32 v114, v125
	v_mov_b32_e32 v105, v125
	v_mov_b32_e32 v104, v125
	v_mov_b32_e32 v103, v125
	v_mov_b32_e32 v102, v125
	v_mov_b32_e32 v101, v125
	v_mov_b32_e32 v100, v125
	v_mov_b32_e32 v99, v125
	v_mov_b32_e32 v98, v125
	v_mov_b32_e32 v89, v125
	v_mov_b32_e32 v88, v125
	v_mov_b32_e32 v87, v125
	v_mov_b32_e32 v86, v125
	v_mov_b32_e32 v85, v125
	v_mov_b32_e32 v84, v125
	v_mov_b32_e32 v83, v125
	v_mov_b32_e32 v82, v125
	v_mov_b32_e32 v73, v125
	v_mov_b32_e32 v72, v125
	v_mov_b32_e32 v71, v125
	v_mov_b32_e32 v70, v125
	v_mov_b32_e32 v69, v125
	v_mov_b32_e32 v68, v125
	v_mov_b32_e32 v67, v125
	v_mov_b32_e32 v66, v125
	v_mov_b32_e32 v65, v125
	v_mov_b32_e32 v64, v125
	v_mov_b32_e32 v63, v125
	v_mov_b32_e32 v62, v125
	v_mov_b32_e32 v61, v125
	v_mov_b32_e32 v60, v125
	v_mov_b32_e32 v59, v125
	v_mov_b32_e32 v58, v125
	v_mov_b32_e32 v49, v125
	v_mov_b32_e32 v48, v125
	v_mov_b32_e32 v47, v125
	v_mov_b32_e32 v46, v125
	v_mov_b32_e32 v45, v125
	v_mov_b32_e32 v44, v125
	v_mov_b32_e32 v43, v125
	v_mov_b32_e32 v42, v125
	v_mov_b32_e32 v33, v125
	v_mov_b32_e32 v32, v125
	v_mov_b32_e32 v31, v125
	v_mov_b32_e32 v30, v125
	v_mov_b32_e32 v29, v125
	v_mov_b32_e32 v28, v125
	v_mov_b32_e32 v27, v125
	v_mov_b32_e32 v26, v125
	v_mov_b32_e32 v17, v125
	v_mov_b32_e32 v16, v125
	v_mov_b32_e32 v15, v125
	v_mov_b32_e32 v14, v125
	v_mov_b32_e32 v13, v125
	v_mov_b32_e32 v12, v125
	v_mov_b32_e32 v11, v125
	v_mov_b32_e32 v10, v125
	v_mov_b32_e32 v57, v125
	v_mov_b32_e32 v56, v125
	v_mov_b32_e32 v55, v125
	v_mov_b32_e32 v54, v125
	v_mov_b32_e32 v53, v125
	v_mov_b32_e32 v52, v125
	v_mov_b32_e32 v51, v125
	v_mov_b32_e32 v50, v125
	v_mov_b32_e32 v41, v125
	v_mov_b32_e32 v40, v125
	v_mov_b32_e32 v39, v125
	v_mov_b32_e32 v38, v125
	v_mov_b32_e32 v37, v125
	v_mov_b32_e32 v36, v125
	v_mov_b32_e32 v35, v125
	v_mov_b32_e32 v34, v125
	v_mov_b32_e32 v25, v125
	v_mov_b32_e32 v24, v125
	v_mov_b32_e32 v23, v125
	v_mov_b32_e32 v22, v125
	v_mov_b32_e32 v21, v125
	v_mov_b32_e32 v20, v125
	v_mov_b32_e32 v19, v125
	v_mov_b32_e32 v18, v125
	v_mov_b32_e32 v9, v125
	v_mov_b32_e32 v8, v125
	v_mov_b32_e32 v7, v125
	v_mov_b32_e32 v6, v125
	v_mov_b32_e32 v5, v125
	v_mov_b32_e32 v4, v125
	v_mov_b32_e32 v3, v125
	v_mov_b32_e32 v2, v125
.Lzs_15:
	s_cbranch_vccnz .LBB0_4647
	s_and_b64 s[40:41], s[0:1], exec
	s_cselect_b32 s25, s29, s39
	s_cselect_b32 s27, s28, s38
	s_cselect_b32 s67, s31, s37
	s_cselect_b32 s68, s30, s36
	s_add_u32 s69, s36, 0x100
	s_addc_u32 s70, s37, 0
	s_add_u32 s36, s38, 0x80080
	v_mov_b32_e32 v2, 0
	s_addc_u32 s37, s39, 0
	s_mov_b32 s38, 0
	v_mov_b32_e32 v3, v2
	v_mov_b32_e32 v4, v2
	v_mov_b32_e32 v5, v2
	v_mov_b32_e32 v6, v2
	v_mov_b32_e32 v7, v2
	v_mov_b32_e32 v8, v2
	v_mov_b32_e32 v9, v2
	v_mov_b32_e32 v18, v2
	v_mov_b32_e32 v19, v2
	v_mov_b32_e32 v20, v2
	v_mov_b32_e32 v21, v2
	v_mov_b32_e32 v22, v2
	v_mov_b32_e32 v23, v2
	v_mov_b32_e32 v24, v2
	v_mov_b32_e32 v25, v2
	v_mov_b32_e32 v34, v2
	v_mov_b32_e32 v35, v2
	v_mov_b32_e32 v36, v2
	v_mov_b32_e32 v37, v2
	v_mov_b32_e32 v38, v2
	v_mov_b32_e32 v39, v2
	v_mov_b32_e32 v40, v2
	v_mov_b32_e32 v41, v2
	v_mov_b32_e32 v50, v2
	v_mov_b32_e32 v51, v2
	v_mov_b32_e32 v52, v2
	v_mov_b32_e32 v53, v2
	v_mov_b32_e32 v54, v2
	v_mov_b32_e32 v55, v2
	v_mov_b32_e32 v56, v2
	v_mov_b32_e32 v57, v2
	v_mov_b32_e32 v10, v2
	v_mov_b32_e32 v11, v2
	v_mov_b32_e32 v12, v2
	v_mov_b32_e32 v13, v2
	v_mov_b32_e32 v14, v2
	v_mov_b32_e32 v15, v2
	v_mov_b32_e32 v16, v2
	v_mov_b32_e32 v17, v2
	v_mov_b32_e32 v26, v2
	v_mov_b32_e32 v27, v2
	v_mov_b32_e32 v28, v2
	v_mov_b32_e32 v29, v2
	v_mov_b32_e32 v30, v2
	v_mov_b32_e32 v31, v2
	v_mov_b32_e32 v32, v2
	v_mov_b32_e32 v33, v2
	v_mov_b32_e32 v42, v2
	v_mov_b32_e32 v43, v2
	v_mov_b32_e32 v44, v2
	v_mov_b32_e32 v45, v2
	v_mov_b32_e32 v46, v2
	v_mov_b32_e32 v47, v2
	v_mov_b32_e32 v48, v2
	v_mov_b32_e32 v49, v2
	v_mov_b32_e32 v58, v2
	v_mov_b32_e32 v59, v2
	v_mov_b32_e32 v60, v2
	v_mov_b32_e32 v61, v2
	v_mov_b32_e32 v62, v2
	v_mov_b32_e32 v63, v2
	v_mov_b32_e32 v64, v2
	v_mov_b32_e32 v65, v2
	v_mov_b32_e32 v66, v2
	v_mov_b32_e32 v67, v2
	v_mov_b32_e32 v68, v2
	v_mov_b32_e32 v69, v2
	v_mov_b32_e32 v70, v2
	v_mov_b32_e32 v71, v2
	v_mov_b32_e32 v72, v2
	v_mov_b32_e32 v73, v2
	v_mov_b32_e32 v82, v2
	v_mov_b32_e32 v83, v2
	v_mov_b32_e32 v84, v2
	v_mov_b32_e32 v85, v2
	v_mov_b32_e32 v86, v2
	v_mov_b32_e32 v87, v2
	v_mov_b32_e32 v88, v2
	v_mov_b32_e32 v89, v2
	v_mov_b32_e32 v98, v2
	v_mov_b32_e32 v99, v2
	v_mov_b32_e32 v100, v2
	v_mov_b32_e32 v101, v2
	v_mov_b32_e32 v102, v2
	v_mov_b32_e32 v103, v2
	v_mov_b32_e32 v104, v2
	v_mov_b32_e32 v105, v2
	v_mov_b32_e32 v114, v2
	v_mov_b32_e32 v115, v2
	v_mov_b32_e32 v116, v2
	v_mov_b32_e32 v117, v2
	v_mov_b32_e32 v118, v2
	v_mov_b32_e32 v119, v2
	v_mov_b32_e32 v120, v2
	v_mov_b32_e32 v121, v2
	v_mov_b32_e32 v74, v2
	v_mov_b32_e32 v75, v2
	v_mov_b32_e32 v76, v2
	v_mov_b32_e32 v77, v2
	v_mov_b32_e32 v78, v2
	v_mov_b32_e32 v79, v2
	v_mov_b32_e32 v80, v2
	v_mov_b32_e32 v81, v2
	v_mov_b32_e32 v90, v2
	v_mov_b32_e32 v91, v2
	v_mov_b32_e32 v92, v2
	v_mov_b32_e32 v93, v2
	v_mov_b32_e32 v94, v2
	v_mov_b32_e32 v95, v2
	v_mov_b32_e32 v96, v2
	v_mov_b32_e32 v97, v2
	v_mov_b32_e32 v106, v2
	v_mov_b32_e32 v107, v2
	v_mov_b32_e32 v108, v2
	v_mov_b32_e32 v109, v2
	v_mov_b32_e32 v110, v2
	v_mov_b32_e32 v111, v2
	v_mov_b32_e32 v112, v2
	v_mov_b32_e32 v113, v2
	v_mov_b32_e32 v126, v2
	v_mov_b32_e32 v127, v2
	v_mov_b32_e32 v128, v2
	v_mov_b32_e32 v129, v2
	v_mov_b32_e32 v122, v2
	v_mov_b32_e32 v123, v2
	v_mov_b32_e32 v124, v2
	v_mov_b32_e32 v125, v2

;     ...
;         for (int t = 0; t < nt; t += 2) {
;     ...
; #pragma unroll
;         for (int a = 0; a < 2; ++a)
; #pragma unroll
;             for (int b = 0; b < 2; ++b)
; #pragma unroll
;                 for (int m = 0; m < 4; ++m)
; #pragma unroll
;                     for (int n = 0; n < 2; ++n) acc[a][b][m][n] = (f32x4){0.f, 0.f, 0.f, 0.f};
.LBB0_4853:
	v_mov_b32_e32 v107, 0
	s_andn2_b64 vcc, exec, s[14:15]
	s_cbranch_vccz .Lzs_17
	v_mov_b32_e32 v106, v107
	v_mov_b32_e32 v105, v107
	v_mov_b32_e32 v104, v107
	v_mov_b32_e32 v111, v107
	v_mov_b32_e32 v110, v107
	v_mov_b32_e32 v109, v107
	v_mov_b32_e32 v108, v107
	v_mov_b32_e32 v123, v107
	v_mov_b32_e32 v122, v107
	v_mov_b32_e32 v121, v107
	v_mov_b32_e32 v120, v107
	v_mov_b32_e32 v131, v107
	v_mov_b32_e32 v130, v107
	v_mov_b32_e32 v129, v107
	v_mov_b32_e32 v128, v107
	v_mov_b32_e32 v147, v107
	v_mov_b32_e32 v146, v107
	v_mov_b32_e32 v145, v107
	v_mov_b32_e32 v144, v107
	v_mov_b32_e32 v151, v107
	v_mov_b32_e32 v150, v107
	v_mov_b32_e32 v149, v107
	v_mov_b32_e32 v148, v107
	v_mov_b32_e32 v155, v107
	v_mov_b32_e32 v154, v107
	v_mov_b32_e32 v153, v107
	v_mov_b32_e32 v152, v107
	v_mov_b32_e32 v159, v107
	v_mov_b32_e32 v158, v107
	v_mov_b32_e32 v157, v107
	v_mov_b32_e32 v156, v107
	v_mov_b32_e32 v99, v107
	v_mov_b32_e32 v98, v107
	v_mov_b32_e32 v97, v107
	v_mov_b32_e32 v96, v107
	v_mov_b32_e32 v103, v107
	v_mov_b32_e32 v102, v107
	v_mov_b32_e32 v101, v107
	v_mov_b32_e32 v100, v107
	v_mov_b32_e32 v115, v107
	v_mov_b32_e32 v114, v107
	v_mov_b32_e32 v113, v107
	v_mov_b32_e32 v112, v107
	v_mov_b32_e32 v119, v107
	v_mov_b32_e32 v118, v107
	v_mov_b32_e32 v117, v107
	v_mov_b32_e32 v116, v107
	v_mov_b32_e32 v127, v107
	v_mov_b32_e32 v126, v107
	v_mov_b32_e32 v125, v107
	v_mov_b32_e32 v124, v107
	v_mov_b32_e32 v135, v107
	v_mov_b32_e32 v134, v107
	v_mov_b32_e32 v133, v107
	v_mov_b32_e32 v132, v107
	v_mov_b32_e32 v139, v107
	v_mov_b32_e32 v138, v107
	v_mov_b32_e32 v137, v107
	v_mov_b32_e32 v136, v107
	v_mov_b32_e32 v143, v107
	v_mov_b32_e32 v142, v107
	v_mov_b32_e32 v141, v107
	v_mov_b32_e32 v140, v107
	v_mov_b32_e32 v43, v107
	v_mov_b32_e32 v42, v107
	v_mov_b32_e32 v41, v107
	v_mov_b32_e32 v40, v107
	v_mov_b32_e32 v47, v107
	v_mov_b32_e32 v46, v107
	v_mov_b32_e32 v45, v107
	v_mov_b32_e32 v44, v107
	v_mov_b32_e32 v59, v107
	v_mov_b32_e32 v58, v107
	v_mov_b32_e32 v57, v107
	v_mov_b32_e32 v56, v107
	v_mov_b32_e32 v63, v107
	v_mov_b32_e32 v62, v107
	v_mov_b32_e32 v61, v107
	v_mov_b32_e32 v60, v107
	v_mov_b32_e32 v75, v107
	v_mov_b32_e32 v74, v107
	v_mov_b32_e32 v73, v107
	v_mov_b32_e32 v72, v107
	v_mov_b32_e32 v79, v107
	v_mov_b32_e32 v78, v107
	v_mov_b32_e32 v77, v107
	v_mov_b32_e32 v76, v107
	v_mov_b32_e32 v91, v107
	v_mov_b32_e32 v90, v107
	v_mov_b32_e32 v89, v107
	v_mov_b32_e32 v88, v107
	v_mov_b32_e32 v95, v107
	v_mov_b32_e32 v94, v107
	v_mov_b32_e32 v93, v107
	v_mov_b32_e32 v92, v107
	v_mov_b32_e32 v35, v107
	v_mov_b32_e32 v34, v107
	v_mov_b32_e32 v33, v107
	v_mov_b32_e32 v32, v107
	v_mov_b32_e32 v39, v107
	v_mov_b32_e32 v38, v107
	v_mov_b32_e32 v37, v107
	v_mov_b32_e32 v36, v107
	v_mov_b32_e32 v51, v107
	v_mov_b32_e32 v50, v107
	v_mov_b32_e32 v49, v107
	v_mov_b32_e32 v48, v107
	v_mov_b32_e32 v55, v107
	v_mov_b32_e32 v54, v107
	v_mov_b32_e32 v53, v107
	v_mov_b32_e32 v52, v107
	v_mov_b32_e32 v67, v107
	v_mov_b32_e32 v66, v107
	v_mov_b32_e32 v65, v107
	v_mov_b32_e32 v64, v107
	v_mov_b32_e32 v71, v107
	v_mov_b32_e32 v70, v107
	v_mov_b32_e32 v69, v107
	v_mov_b32_e32 v68, v107
	v_mov_b32_e32 v83, v107
	v_mov_b32_e32 v82, v107
	v_mov_b32_e32 v81, v107
	v_mov_b32_e32 v80, v107
	v_mov_b32_e32 v87, v107
	v_mov_b32_e32 v86, v107
	v_mov_b32_e32 v85, v107
	v_mov_b32_e32 v84, v107
.Lzs_17:
	s_cbranch_vccnz .LBB0_4856
	s_add_u32 s59, s24, 0x100
	v_mov_b32_e32 v84, 0
	s_addc_u32 s60, s25, 0
	s_mov_b32 s26, 0
	v_mov_b32_e32 v85, v84
	v_mov_b32_e32 v86, v84
	v_mov_b32_e32 v87, v84
	v_mov_b32_e32 v80, v84
	v_mov_b32_e32 v81, v84
	v_mov_b32_e32 v82, v84
	v_mov_b32_e32 v83, v84
	v_mov_b32_e32 v68, v84
	v_mov_b32_e32 v69, v84
	v_mov_b32_e32 v70, v84
	v_mov_b32_e32 v71, v84
	v_mov_b32_e32 v64, v84
	v_mov_b32_e32 v65, v84
	v_mov_b32_e32 v66, v84
	v_mov_b32_e32 v67, v84
	v_mov_b32_e32 v52, v84
	v_mov_b32_e32 v53, v84
	v_mov_b32_e32 v54, v84
	v_mov_b32_e32 v55, v84
	v_mov_b32_e32 v48, v84
	v_mov_b32_e32 v49, v84
	v_mov_b32_e32 v50, v84
	v_mov_b32_e32 v51, v84
	v_mov_b32_e32 v36, v84
	v_mov_b32_e32 v37, v84
	v_mov_b32_e32 v38, v84
	v_mov_b32_e32 v39, v84
	v_mov_b32_e32 v32, v84
	v_mov_b32_e32 v33, v84
	v_mov_b32_e32 v34, v84
	v_mov_b32_e32 v35, v84
	v_mov_b32_e32 v92, v84
	v_mov_b32_e32 v93, v84
	v_mov_b32_e32 v94, v84
	v_mov_b32_e32 v95, v84
	v_mov_b32_e32 v88, v84
	v_mov_b32_e32 v89, v84
	v_mov_b32_e32 v90, v84
	v_mov_b32_e32 v91, v84
	v_mov_b32_e32 v76, v84
	v_mov_b32_e32 v77, v84
	v_mov_b32_e32 v78, v84
	v_mov_b32_e32 v79, v84
	v_mov_b32_e32 v72, v84
	v_mov_b32_e32 v73, v84
	v_mov_b32_e32 v74, v84
	v_mov_b32_e32 v75, v84
	v_mov_b32_e32 v60, v84
	v_mov_b32_e32 v61, v84
	v_mov_b32_e32 v62, v84
	v_mov_b32_e32 v63, v84
	v_mov_b32_e32 v56, v84
	v_mov_b32_e32 v57, v84
	v_mov_b32_e32 v58, v84
	v_mov_b32_e32 v59, v84
	v_mov_b32_e32 v44, v84
	v_mov_b32_e32 v45, v84
	v_mov_b32_e32 v46, v84
	v_mov_b32_e32 v47, v84
	v_mov_b32_e32 v40, v84
	v_mov_b32_e32 v41, v84
	v_mov_b32_e32 v42, v84
	v_mov_b32_e32 v43, v84
	v_mov_b32_e32 v140, v84
	v_mov_b32_e32 v141, v84
	v_mov_b32_e32 v142, v84
	v_mov_b32_e32 v143, v84
	v_mov_b32_e32 v136, v84
	v_mov_b32_e32 v137, v84
	v_mov_b32_e32 v138, v84
	v_mov_b32_e32 v139, v84
	v_mov_b32_e32 v132, v84
	v_mov_b32_e32 v133, v84
	v_mov_b32_e32 v134, v84
	v_mov_b32_e32 v135, v84
	v_mov_b32_e32 v124, v84
	v_mov_b32_e32 v125, v84
	v_mov_b32_e32 v126, v84
	v_mov_b32_e32 v127, v84
	v_mov_b32_e32 v116, v84
	v_mov_b32_e32 v117, v84
	v_mov_b32_e32 v118, v84
	v_mov_b32_e32 v119, v84
	v_mov_b32_e32 v112, v84
	v_mov_b32_e32 v113, v84
	v_mov_b32_e32 v114, v84
	v_mov_b32_e32 v115, v84
	v_mov_b32_e32 v100, v84
	v_mov_b32_e32 v101, v84
	v_mov_b32_e32 v102, v84
	v_mov_b32_e32 v103, v84
	v_mov_b32_e32 v96, v84
	v_mov_b32_e32 v97, v84
	v_mov_b32_e32 v98, v84
	v_mov_b32_e32 v99, v84
	v_mov_b32_e32 v156, v84
	v_mov_b32_e32 v157, v84
	v_mov_b32_e32 v158, v84
	v_mov_b32_e32 v159, v84
	v_mov_b32_e32 v152, v84
	v_mov_b32_e32 v153, v84
	v_mov_b32_e32 v154, v84
	v_mov_b32_e32 v155, v84
	v_mov_b32_e32 v148, v84
	v_mov_b32_e32 v149, v84
	v_mov_b32_e32 v150, v84
	v_mov_b32_e32 v151, v84
	v_mov_b32_e32 v144, v84
	v_mov_b32_e32 v145, v84
	v_mov_b32_e32 v146, v84
	v_mov_b32_e32 v147, v84
	v_mov_b32_e32 v128, v84
	v_mov_b32_e32 v129, v84
	v_mov_b32_e32 v130, v84
	v_mov_b32_e32 v131, v84
	v_mov_b32_e32 v120, v84
	v_mov_b32_e32 v121, v84
	v_mov_b32_e32 v122, v84
	v_mov_b32_e32 v123, v84
	v_mov_b32_e32 v108, v84
	v_mov_b32_e32 v109, v84
	v_mov_b32_e32 v110, v84
	v_mov_b32_e32 v111, v84
	v_mov_b32_e32 v104, v84
	v_mov_b32_e32 v105, v84
	v_mov_b32_e32 v106, v84
	v_mov_b32_e32 v107, v84
